# GLA chunk loops: the packed v_pk_mul_f32 state-decay multiplies beside the state-update MFMAs split into scalar v_mul_f32 pairs, on top of v024
# speedup vs baseline: 1.0010x; 1.0010x over previous
; #define LAS __attribute__((address_space(3)))
; __device__ __forceinline__ void gla_unit(LAS unsigned char* lds, const unsigned char* ws, const float* g_onorm, const int b, const int h, const int wv) {
;     ...
;         f32x16 O[2];
; #pragma unroll
;         for (int tt = 0; tt < 2; ++tt)
; #pragma unroll
;             for (int r = 0; r < 16; ++r) O[tt][r] = 0.f;
; #pragma unroll
;         for (int et = 0; et < 4; ++et)
; #pragma unroll
;             for (int s2 = 0; s2 < 2; ++s2) {
;                 const bf16x8 sb = pack8(S[et], s2);
; #pragma unroll
;                 for (int tt = 0; tt < 2; ++tt) {
;                     const bf16x8 aq = ld2x64(qb8 + 32 * tt * QS + (32 * et + 16 * s2) * 2);
;                     O[tt] = __builtin_amdgcn_mfma_f32_32x32x16_bf16(aq, sb, O[tt], 0, 0, 0);
;                 }
;             }
;         __syncthreads();
; #pragma unroll
;         for (int pr = 0; pr < 3; ++pr) {
;             const int st = (pr == 2) ? 1 : 0, tt = (pr == 0) ? 0 : 1;
; #pragma unroll
;             for (int s2 = 0; s2 < 2; ++s2) {
;                 const bf16x8 ax = *(const LAS bf16x8*)(frb + (pr * 2 + s2) * 1024);
;                 const LAS unsigned char* vp = vP + (32 * st + 16 * s2) * VS;
;                 const bf16x8 bv = tr8(vp, vp + 8 * VS);
;                 O[tt] = __builtin_amdgcn_mfma_f32_32x32x16_bf16(ax, bv, O[tt], 0, 0, 0);
;             }
;         }
;         __builtin_amdgcn_sched_barrier(0);
; #pragma unroll
;         for (int tt = 0; tt < 2; ++tt)
; #pragma unroll
;             for (int r = 0; r < 16; ++r) ob[(32 * tt + (r & 3) + 8 * (r >> 2)) * OS] = O[tt][r];
;         __builtin_amdgcn_sched_barrier(0);
; #pragma unroll
;         for (int et = 0; et < 4; ++et)
; #pragma unroll
;             for (int rg = 0; rg < 4; ++rg) { const f32x4 dl = *(const LAS f32x4*)&decb[32 * et + 8 * rg];
.LBB0_635:
	ds_read2_b64 v[64:67], v222 offset1:2
	v_cvt_pk_bf16_f32 v68, v32, v33
	v_cvt_pk_bf16_f32 v69, v34, v35
	v_cvt_pk_bf16_f32 v70, v36, v37
	v_cvt_pk_bf16_f32 v71, v38, v39
	ds_read2_b64 v[192:195], v222 offset0:4 offset1:6
	v_cvt_pk_bf16_f32 v196, v40, v41
	v_cvt_pk_bf16_f32 v197, v42, v43
	v_cvt_pk_bf16_f32 v198, v44, v45
	s_waitcnt lgkmcnt(1)
	v_mfma_f32_32x32x16_bf16 v[80:95], v[64:67], v[68:71], 0
	ds_read2_b64 v[64:67], v223 offset0:64 offset1:66
	v_cvt_pk_bf16_f32 v199, v46, v47
	s_waitcnt lgkmcnt(1)
	s_nop 0
	v_mfma_f32_32x32x16_bf16 v[80:95], v[192:195], v[196:199], v[80:95]
	ds_read2_b64 v[192:195], v223 offset0:68 offset1:70
	s_waitcnt lgkmcnt(1)
	v_mfma_f32_32x32x16_bf16 v[64:79], v[64:67], v[68:71], 0
	s_waitcnt lgkmcnt(0)
	v_mfma_f32_32x32x16_bf16 v[64:79], v[192:195], v[196:199], v[64:79]
	ds_read2_b64 v[192:195], v222 offset0:8 offset1:10
	ds_read2_b64 v[224:227], v223 offset0:72 offset1:74
	ds_read2_b64 v[232:235], v222 offset0:12 offset1:14
	v_cvt_pk_bf16_f32 v196, v16, v17
	v_cvt_pk_bf16_f32 v197, v18, v19
	v_cvt_pk_bf16_f32 v198, v20, v21
	v_cvt_pk_bf16_f32 v199, v22, v23
	s_waitcnt lgkmcnt(2)
	s_nop 0
	v_mfma_f32_32x32x16_bf16 v[80:95], v[192:195], v[196:199], v[80:95]
	ds_read2_b64 v[236:239], v223 offset0:76 offset1:78
	s_waitcnt lgkmcnt(2)
	v_mfma_f32_32x32x16_bf16 v[64:79], v[224:227], v[196:199], v[64:79]
	ds_read2_b64 v[192:195], v222 offset0:16 offset1:18
	v_cvt_pk_bf16_f32 v196, v24, v25
	v_cvt_pk_bf16_f32 v197, v26, v27
	v_cvt_pk_bf16_f32 v198, v28, v29
	v_cvt_pk_bf16_f32 v199, v30, v31
	s_waitcnt lgkmcnt(2)
	s_nop 0
	v_mfma_f32_32x32x16_bf16 v[80:95], v[232:235], v[196:199], v[80:95]
	ds_read2_b64 v[224:227], v223 offset0:80 offset1:82
	s_waitcnt lgkmcnt(2)
	v_mfma_f32_32x32x16_bf16 v[64:79], v[236:239], v[196:199], v[64:79]
	ds_read2_b64 v[232:235], v222 offset0:20 offset1:22
	v_cvt_pk_bf16_f32 v196, v48, v49
	v_cvt_pk_bf16_f32 v197, v50, v51
	v_cvt_pk_bf16_f32 v198, v52, v53
	v_cvt_pk_bf16_f32 v199, v54, v55
	s_waitcnt lgkmcnt(2)
	s_nop 0
	v_mfma_f32_32x32x16_bf16 v[80:95], v[192:195], v[196:199], v[80:95]
	ds_read2_b64 v[236:239], v223 offset0:84 offset1:86
	s_waitcnt lgkmcnt(2)
	v_mfma_f32_32x32x16_bf16 v[64:79], v[224:227], v[196:199], v[64:79]
	ds_read2_b64 v[192:195], v222 offset0:24 offset1:26
	v_cvt_pk_bf16_f32 v196, v56, v57
	v_cvt_pk_bf16_f32 v197, v58, v59
	v_cvt_pk_bf16_f32 v198, v60, v61
	v_cvt_pk_bf16_f32 v199, v62, v63
	s_waitcnt lgkmcnt(2)
	s_nop 0
	v_mfma_f32_32x32x16_bf16 v[80:95], v[232:235], v[196:199], v[80:95]
	ds_read2_b64 v[224:227], v223 offset0:88 offset1:90
	s_waitcnt lgkmcnt(2)
	v_mfma_f32_32x32x16_bf16 v[64:79], v[236:239], v[196:199], v[64:79]
	ds_read2_b64 v[232:235], v222 offset0:28 offset1:30
	v_cvt_pk_bf16_f32 v196, v0, v1
	v_cvt_pk_bf16_f32 v197, v2, v3
	v_cvt_pk_bf16_f32 v198, v4, v5
	v_cvt_pk_bf16_f32 v199, v6, v7
	s_waitcnt lgkmcnt(2)
	s_nop 0
	v_mfma_f32_32x32x16_bf16 v[80:95], v[192:195], v[196:199], v[80:95]
	ds_read2_b64 v[236:239], v223 offset0:92 offset1:94
	s_waitcnt lgkmcnt(2)
	v_mfma_f32_32x32x16_bf16 v[64:79], v[224:227], v[196:199], v[64:79]
	v_cvt_pk_bf16_f32 v196, v8, v9
	v_cvt_pk_bf16_f32 v197, v10, v11
	v_cvt_pk_bf16_f32 v198, v12, v13
	v_cvt_pk_bf16_f32 v199, v14, v15
	s_waitcnt lgkmcnt(1)
	s_nop 0
	v_mfma_f32_32x32x16_bf16 v[80:95], v[232:235], v[196:199], v[80:95]
	s_waitcnt lgkmcnt(0)
	s_barrier
	v_mfma_f32_32x32x16_bf16 v[64:79], v[236:239], v[196:199], v[64:79]
	ds_read_b128 v[192:195], v206
	ds_read_b64_tr_b16 v[196:197], v218
	ds_read_b64_tr_b16 v[198:199], v218 offset:4608
	ds_read_b128 v[222:225], v206 offset:1024
	ds_read_b64_tr_b16 v[226:227], v218 offset:9216
	ds_read_b64_tr_b16 v[228:229], v218 offset:13824
	s_waitcnt lgkmcnt(3)
	v_mfma_f32_32x32x16_bf16 v[80:95], v[192:195], v[196:199], v[80:95]
	s_waitcnt lgkmcnt(0)
	v_mfma_f32_32x32x16_bf16 v[80:95], v[222:225], v[226:229], v[80:95]
	ds_read_b128 v[192:195], v206 offset:2048
	ds_read_b128 v[222:225], v206 offset:3072
	s_waitcnt lgkmcnt(1)
	v_mfma_f32_32x32x16_bf16 v[64:79], v[192:195], v[196:199], v[64:79]
	s_waitcnt lgkmcnt(0)
	v_mfma_f32_32x32x16_bf16 v[64:79], v[222:225], v[226:229], v[64:79]
	ds_read_b128 v[192:195], v206 offset:4096
	ds_read_b64_tr_b16 v[196:197], v218 offset:18432
	ds_read_b64_tr_b16 v[198:199], v218 offset:23040
	ds_read_b128 v[222:225], v206 offset:5120
	ds_read_b64_tr_b16 v[226:227], v218 offset:27648
	ds_read_b64_tr_b16 v[228:229], v218 offset:32256
	s_waitcnt lgkmcnt(3)
	v_mfma_f32_32x32x16_bf16 v[64:79], v[192:195], v[196:199], v[64:79]
	s_waitcnt lgkmcnt(0)
	v_mfma_f32_32x32x16_bf16 v[64:79], v[222:225], v[226:229], v[64:79]
	ds_write_b32 v207, v80
	ds_write_b32 v207, v81 offset:1040
	ds_write_b32 v207, v82 offset:2080
	ds_write_b32 v207, v83 offset:3120
	ds_write_b32 v207, v84 offset:8320
	ds_write_b32 v207, v85 offset:9360
	ds_write_b32 v207, v86 offset:10400
	ds_write_b32 v207, v87 offset:11440
	ds_write_b32 v207, v88 offset:16640
	ds_write_b32 v207, v89 offset:17680
	ds_write_b32 v207, v90 offset:18720
	ds_write_b32 v207, v91 offset:19760
	ds_write_b32 v207, v92 offset:24960
	ds_write_b32 v207, v93 offset:26000
	ds_write_b32 v207, v94 offset:27040
	ds_write_b32 v207, v95 offset:28080
	ds_write_b32 v207, v64 offset:33280
	ds_write_b32 v207, v65 offset:34320
	ds_write_b32 v207, v66 offset:35360
	ds_write_b32 v207, v67 offset:36400
	ds_write_b32 v207, v68 offset:41600
	ds_write_b32 v207, v69 offset:42640
	ds_write_b32 v207, v70 offset:43680
	ds_write_b32 v207, v71 offset:44720
	ds_write_b32 v207, v72 offset:49920
	ds_write_b32 v207, v73 offset:50960
	ds_write_b32 v207, v74 offset:52000
	ds_write_b32 v207, v75 offset:53040
	ds_write_b32 v207, v76 offset:58240
	ds_write_b32 v207, v77 offset:59280
	ds_write_b32 v207, v78 offset:60320
	ds_write_b32 v207, v79 offset:61360
	ds_read_b128 v[64:67], v205 offset:96
	ds_read_b128 v[68:71], v205 offset:64
	ds_read_b128 v[72:75], v205 offset:32
	ds_read_b128 v[76:79], v205
	s_waitcnt vmcnt(11)
; #define LAS __attribute__((address_space(3)))
; __device__ __forceinline__ void gla_unit(LAS unsigned char* lds, const unsigned char* ws, const float* g_onorm, const int b, const int h, const int wv) {
;     ...
; #pragma unroll
;         for (int et = 0; et < 4; ++et)
; #pragma unroll
;             for (int rg = 0; rg < 4; ++rg) { const f32x4 dl = *(const LAS f32x4*)&decb[32 * et + 8 * rg];
; #pragma unroll
;                 for (int x = 0; x < 4; ++x) S[et][4 * rg + x] *= dl[x]; }
; #pragma unroll
;         for (int ks = 0; ks < 4; ++ks) {
;             const LAS unsigned char* vp = vN + 16 * ks * VS;
;             const bf16x8 bv = tr8(vp, vp + 4 * VS);
; #pragma unroll
;             for (int et = 0; et < 4; ++et) {
;                 const LAS unsigned char* kp = keN + 32 * et * 2 + 16 * ks * ES;
;                 const bf16x8 ak = tr8(kp, kp + 4 * ES);
;                 S[et] = __builtin_amdgcn_mfma_f32_32x32x16_bf16(ak, bv, S[et], 0, 0, 0);
;             }
;         }
	v_lshlrev_b32_e32 v232, 16, v176
	s_waitcnt lgkmcnt(3)
	v_mul_f32_e32 v46, v46, v66
	v_mul_f32_e32 v47, v47, v67
	s_waitcnt lgkmcnt(2)
	v_mul_f32_e32 v42, v42, v70
	v_mul_f32_e32 v43, v43, v71
	v_mul_f32_e32 v44, v44, v64
	v_mul_f32_e32 v45, v45, v65
	s_waitcnt lgkmcnt(0)
	v_mul_f32_e32 v34, v34, v78
	v_mul_f32_e32 v35, v35, v79
	v_mul_f32_e32 v40, v40, v68
	v_mul_f32_e32 v41, v41, v69
	ds_read_b128 v[68:71], v205 offset:192
	ds_read_b128 v[78:81], v205 offset:224
	ds_read_b128 v[64:67], v205 offset:128
	ds_read_b128 v[82:85], v205 offset:160
	v_mul_f32_e32 v38, v38, v74
	v_mul_f32_e32 v39, v39, v75
	v_mul_f32_e32 v36, v36, v72
	v_mul_f32_e32 v37, v37, v73
	v_mul_f32_e32 v32, v32, v76
	v_mul_f32_e32 v33, v33, v77
	s_waitcnt lgkmcnt(2)
	v_mul_f32_e32 v30, v30, v80
	v_mul_f32_e32 v31, v31, v81
	v_mul_f32_e32 v26, v26, v70
	v_mul_f32_e32 v27, v27, v71
	s_waitcnt lgkmcnt(0)
	v_mul_f32_e32 v22, v22, v84
	v_mul_f32_e32 v23, v23, v85
	v_mul_f32_e32 v18, v18, v66
	v_mul_f32_e32 v19, v19, v67
	v_mul_f32_e32 v28, v28, v78
	v_mul_f32_e32 v29, v29, v79
	v_mul_f32_e32 v24, v24, v68
	v_mul_f32_e32 v25, v25, v69
	v_mul_f32_e32 v20, v20, v82
	v_mul_f32_e32 v21, v21, v83
	ds_read_b128 v[66:69], v205 offset:256
	ds_read_b128 v[70:73], v205 offset:288
	ds_read_b128 v[74:77], v205 offset:320
	ds_read_b128 v[78:81], v205 offset:352
	ds_read_b64_tr_b16 v[82:83], v219
	ds_read_b64_tr_b16 v[84:85], v219 offset:2304
	ds_read_b64_tr_b16 v[88:89], v220 offset:1280
	ds_read_b64_tr_b16 v[86:87], v220
	ds_read_b64_tr_b16 v[90:91], v220 offset:64
	ds_read_b64_tr_b16 v[192:193], v220 offset:128
	ds_read_b64_tr_b16 v[196:197], v220 offset:192
	ds_read_b64_tr_b16 v[92:93], v220 offset:1344
	ds_read_b64_tr_b16 v[194:195], v220 offset:1408
	ds_read_b64_tr_b16 v[198:199], v220 offset:1472
	ds_read_b64_tr_b16 v[222:223], v219 offset:9216
	ds_read_b64_tr_b16 v[224:225], v219 offset:11520
	s_waitcnt lgkmcnt(8)
	v_mfma_f32_32x32x16_bf16 v[32:47], v[86:89], v[82:85], v[32:47]
	v_mul_f32_e64 v58, v58, v76
	v_mul_f32_e64 v59, v59, v77
	v_mul_f32_e64 v54, v54, v72
	v_mul_f32_e64 v55, v55, v73
	v_mul_f32_e64 v50, v50, v68
	v_mul_f32_e64 v51, v51, v69
	v_mul_f32_e32 v60, v60, v78
	v_mul_f32_e32 v61, v61, v79
	v_mul_f32_e32 v56, v56, v74
	v_mul_f32_e32 v57, v57, v75
	ds_read_b128 v[72:75], v205 offset:448
	ds_read_b128 v[76:79], v205 offset:480
	v_mul_f32_e32 v52, v52, v70
	v_mul_f32_e32 v53, v53, v71
	ds_read_b128 v[68:71], v205 offset:384
	ds_read_b128 v[86:89], v205 offset:416
	v_mul_f32_e32 v16, v16, v64
	v_mul_f32_e32 v17, v17, v65
	v_mul_f32_e32 v62, v62, v80
	v_mul_f32_e32 v63, v63, v81
	v_mul_f32_e32 v48, v48, v66
	v_mul_f32_e32 v49, v49, v67
	s_waitcnt lgkmcnt(2)
	v_mul_f32_e32 v14, v14, v78
	v_mul_f32_e32 v15, v15, v79
	v_mul_f32_e32 v10, v10, v74
	v_mul_f32_e32 v11, v11, v75
	s_waitcnt lgkmcnt(0)
	v_mul_f32_e32 v6, v6, v88
	v_mul_f32_e32 v7, v7, v89
	v_mul_f32_e32 v2, v2, v70
	v_mul_f32_e32 v3, v3, v71
	v_mul_f32_e32 v12, v12, v76
	v_mul_f32_e32 v13, v13, v77
	v_mul_f32_e32 v8, v8, v72
	v_mul_f32_e32 v9, v9, v73
	v_mul_f32_e32 v4, v4, v86
	v_mul_f32_e32 v5, v5, v87
	v_mul_f32_e32 v0, v0, v68
	v_mul_f32_e32 v1, v1, v69
	v_mfma_f32_32x32x16_bf16 v[16:31], v[90:93], v[82:85], v[16:31]
	ds_read_b64_tr_b16 v[66:67], v220 offset:6400
	ds_read_b64_tr_b16 v[64:65], v220 offset:5120
	ds_read_b64_tr_b16 v[68:69], v220 offset:5184
	ds_read_b64_tr_b16 v[72:73], v220 offset:5248
	ds_read_b64_tr_b16 v[76:77], v220 offset:5312
	ds_read_b64_tr_b16 v[70:71], v220 offset:6464
	ds_read_b64_tr_b16 v[74:75], v220 offset:6528
	ds_read_b64_tr_b16 v[78:79], v220 offset:6592
	v_and_b32_e32 v233, 0xffff0000, v176
	s_mov_b32 s2, 0x4e1c8000
	s_add_i32 s60, s60, 2
	v_lshl_add_u64 v[184:185], v[184:185], 0, s[68:69]
	v_lshl_add_u64 v[188:189], v[188:189], 0, s[70:71]
	s_cmp_lt_u32 s66, 30
	v_mfma_f32_32x32x16_bf16 v[48:63], v[192:195], v[82:85], v[48:63]
	v_lshl_add_u64 v[190:191], v[190:191], 0, s[68:69]
	v_mfma_f32_32x32x16_bf16 v[0:15], v[196:199], v[82:85], v[0:15]
	s_waitcnt lgkmcnt(6)
	v_mfma_f32_32x32x16_bf16 v[32:47], v[64:67], v[222:225], v[32:47]
	s_waitcnt lgkmcnt(2)
	v_mfma_f32_32x32x16_bf16 v[16:31], v[68:71], v[222:225], v[16:31]
	s_waitcnt lgkmcnt(1)
	v_mfma_f32_32x32x16_bf16 v[48:63], v[72:75], v[222:225], v[48:63]
	s_waitcnt lgkmcnt(0)
	v_mfma_f32_32x32x16_bf16 v[0:15], v[76:79], v[222:225], v[0:15]
	ds_read_b64_tr_b16 v[64:65], v219 offset:18432
	ds_read_b64_tr_b16 v[66:67], v219 offset:20736
	ds_read_b64_tr_b16 v[70:71], v220 offset:11520
	ds_read_b64_tr_b16 v[68:69], v220 offset:10240
	ds_read_b64_tr_b16 v[72:73], v220 offset:10304
	ds_read_b64_tr_b16 v[76:77], v220 offset:10368
	ds_read_b64_tr_b16 v[80:81], v220 offset:10432
	ds_read_b64_tr_b16 v[74:75], v220 offset:11584
	ds_read_b64_tr_b16 v[78:79], v220 offset:11648
	ds_read_b64_tr_b16 v[82:83], v220 offset:11712
	ds_read_b64_tr_b16 v[84:85], v219 offset:27648
	ds_read_b64_tr_b16 v[86:87], v219 offset:29952
	s_waitcnt lgkmcnt(8)
	v_mfma_f32_32x32x16_bf16 v[32:47], v[68:71], v[64:67], v[32:47]
	ds_read_b64_tr_b16 v[68:69], v220 offset:16640
	s_waitcnt lgkmcnt(5)
	v_mfma_f32_32x32x16_bf16 v[16:31], v[72:75], v[64:67], v[16:31]
	s_waitcnt lgkmcnt(4)
	v_mfma_f32_32x32x16_bf16 v[48:63], v[76:79], v[64:67], v[48:63]
	s_waitcnt lgkmcnt(3)
	v_mfma_f32_32x32x16_bf16 v[0:15], v[80:83], v[64:67], v[0:15]
	ds_read_b64_tr_b16 v[66:67], v220 offset:15360
	ds_read_b64_tr_b16 v[70:71], v220 offset:15424
	ds_read_b64_tr_b16 v[74:75], v220 offset:15488
	ds_read_b64_tr_b16 v[78:79], v220 offset:15552
	ds_read_b64_tr_b16 v[72:73], v220 offset:16704
	ds_read_b64_tr_b16 v[76:77], v220 offset:16768
	ds_read_b64_tr_b16 v[80:81], v220 offset:16832
	s_waitcnt lgkmcnt(0)
	s_barrier
; #define LAS __attribute__((address_space(3)))
; __device__ __forceinline__ unsigned cvt_pk_bf16(float lo, float hi) { const bf16x2_t r = __builtin_convertvector((f32x2_t){lo, hi}, bf16x2_t); return __builtin_bit_cast(unsigned, r); }
; __device__ __forceinline__ float bf_lo(unsigned w) { return __uint_as_float(w << 16); }
; __device__ __forceinline__ float bf_hi(unsigned w) { return __uint_as_float(w & 0xffff0000u); }
; __device__ __forceinline__ void gla_unit(LAS unsigned char* lds, const unsigned char* ws, const float* g_onorm, const int b, const int h, const int wv) {
;     ...
;         {
;             const int t = tid >> 3, g8 = tid & 7;
;             float ov[32]; float ss = 0.f;
; #pragma unroll
;             for (int x = 0; x < 8; ++x) { const f32x4 v = *(const LAS f32x4*)&obuf[t * OS + 32 * g8 + 4 * x]; ov[4 * x] = v[0]; ov[4 * x + 1] = v[1]; ov[4 * x + 2] = v[2]; ov[4 * x + 3] = v[3];
;                 ss += v[0] * v[0] + v[1] * v[1] + v[2] * v[2] + v[3] * v[3]; }
;             ss += __builtin_bit_cast(float, __builtin_amdgcn_ds_swizzle(__builtin_bit_cast(int, ss), (1 << 10) | 0x1F)); ss += __builtin_bit_cast(float, __builtin_amdgcn_ds_swizzle(__builtin_bit_cast(int, ss), (2 << 10) | 0x1F));
;             ss += __builtin_bit_cast(float, __builtin_amdgcn_ds_swizzle(__builtin_bit_cast(int, ss), (4 << 10) | 0x1F));
;             const float rstd = __builtin_amdgcn_rsqf(ss * (1.0f / 256.0f) + EPSV);
;             bf16_t* mp = mix + (t0 + t) * DM + 1024 + h * 256 + 32 * g8;
; #pragma unroll
;             for (int x = 0; x < 4; ++x) {
;                 const u32x4 og = ogr[x];
;                 const f32x4 g0 = *(const LAS f32x4*)&gon[32 * g8 + 8 * x], g1 = *(const LAS f32x4*)&gon[32 * g8 + 8 * x + 4];
;                 const float gg2[8] = {g0[0], g0[1], g0[2], g0[3], g1[0], g1[1], g1[2], g1[3]};
;                 float res[8];
; #pragma unroll
;                 for (int y = 0; y < 4; ++y) { const float a0 = bf_lo(og[y]), a1 = bf_hi(og[y]);
;                     res[2 * y] = ov[8 * x + 2 * y] * rstd * gg2[2 * y] * a0;
;                     res[2 * y + 1] = ov[8 * x + 2 * y + 1] * rstd * gg2[2 * y + 1] * a1; }
;                 u32x4 wv4; wv4[0] = cvt_pk_bf16(res[0], res[1]); wv4[1] = cvt_pk_bf16(res[2], res[3]); wv4[2] = cvt_pk_bf16(res[4], res[5]); wv4[3] = cvt_pk_bf16(res[6], res[7]);
;                 *(u32x4*)(mp + 8 * x) = wv4;
;             }
	v_mfma_f32_32x32x16_bf16 v[32:47], v[66:69], v[84:87], v[32:47]
	ds_read_b128 v[64:67], v221
	ds_read_b128 v[88:91], v221 offset:16
	ds_read_b128 v[92:95], v221 offset:32
	ds_read_b128 v[192:195], v221 offset:48
	s_waitcnt lgkmcnt(3)
	v_mul_f32_e32 v68, v65, v65
	s_waitcnt lgkmcnt(2)
	v_mul_f32_e32 v69, v89, v89
	v_fmac_f32_e32 v68, v64, v64
	v_fmac_f32_e32 v69, v88, v88
	v_fmac_f32_e32 v68, v66, v66
	v_fmac_f32_e32 v69, v90, v90
	v_mfma_f32_32x32x16_bf16 v[16:31], v[70:73], v[84:87], v[16:31]
	v_fmac_f32_e32 v68, v67, v67
	v_fmac_f32_e32 v69, v91, v91
	s_waitcnt lgkmcnt(1)
	v_mov_b32_e32 v70, v93
	s_waitcnt lgkmcnt(0)
	v_mov_b32_e32 v71, v193
	v_add_f32_e32 v222, v68, v69
	v_mov_b32_e32 v68, v92
	v_mov_b32_e32 v69, v192
	v_pk_mul_f32 v[70:71], v[70:71], v[70:71]
	v_mov_b32_e32 v82, v95
	v_pk_fma_f32 v[68:69], v[68:69], v[68:69], v[70:71]
	v_mov_b32_e32 v70, v94
	v_mov_b32_e32 v71, v194
	v_pk_fma_f32 v[72:73], v[70:71], v[70:71], v[68:69]
	ds_read_b128 v[68:71], v221 offset:64
	ds_read_b128 v[196:199], v221 offset:80
	v_mov_b32_e32 v83, v195
	v_pk_fma_f32 v[72:73], v[82:83], v[82:83], v[72:73]
	v_mfma_f32_32x32x16_bf16 v[48:63], v[74:77], v[84:87], v[48:63]
	v_add_f32_e32 v72, v222, v72
	s_waitcnt lgkmcnt(1)
	v_mov_b32_e32 v82, v69
	s_waitcnt lgkmcnt(0)
	v_mov_b32_e32 v83, v197
	ds_read_b128 v[222:225], v221 offset:96
	ds_read_b128 v[226:229], v221 offset:112
	v_add_f32_e32 v230, v72, v73
	v_mov_b32_e32 v72, v68
	v_mov_b32_e32 v73, v196
	v_pk_mul_f32 v[82:83], v[82:83], v[82:83]
	v_mfma_f32_32x32x16_bf16 v[0:15], v[78:81], v[84:87], v[0:15]
	v_fma_f32 v72, v72, v72, v82
	v_fma_f32 v73, v73, v73, v83
	v_mov_b32_e32 v82, v70
	v_mov_b32_e32 v83, v198
	v_fma_f32 v72, v82, v82, v72
	v_fma_f32 v73, v83, v83, v73
	v_mov_b32_e32 v82, v71
	v_mov_b32_e32 v83, v199
	v_pk_fma_f32 v[72:73], v[82:83], v[82:83], v[72:73]
	s_waitcnt lgkmcnt(1)
	v_mov_b32_e32 v82, v223
	v_add_f32_e32 v72, v230, v72
	s_waitcnt lgkmcnt(0)
	v_mov_b32_e32 v83, v227
	v_add_f32_e32 v230, v72, v73
	v_mov_b32_e32 v72, v222
	v_mov_b32_e32 v73, v226
	v_pk_mul_f32 v[82:83], v[82:83], v[82:83]
	s_nop 0
	v_pk_fma_f32 v[72:73], v[72:73], v[72:73], v[82:83]
	v_mov_b32_e32 v82, v224
	v_mov_b32_e32 v83, v228
	v_pk_fma_f32 v[72:73], v[82:83], v[82:83], v[72:73]
	v_mov_b32_e32 v82, v225
	v_mov_b32_e32 v83, v229
	v_pk_fma_f32 v[72:73], v[82:83], v[82:83], v[72:73]
	s_nop 0
	v_add_f32_e32 v72, v230, v72
	v_add_f32_e32 v72, v72, v73
	ds_swizzle_b32 v73, v72 offset:swizzle(SWAP,1)
	s_waitcnt lgkmcnt(0)
	v_add_f32_e32 v72, v72, v73
	ds_swizzle_b32 v73, v72 offset:swizzle(SWAP,2)
	s_waitcnt lgkmcnt(0)
	v_add_f32_e32 v72, v72, v73
	ds_swizzle_b32 v73, v72 offset:swizzle(SWAP,4)
	s_waitcnt lgkmcnt(0)
	v_add_f32_e32 v72, v72, v73
	v_fmamk_f32 v72, v72, 0x3b800000, v181
	v_rsq_f32_e32 v230, v72
	ds_read_b128 v[72:75], v208
	ds_read_b128 v[76:79], v208 offset:16
	ds_read_b128 v[80:83], v208 offset:32
	ds_read_b128 v[84:87], v208 offset:48
	v_pk_mul_f32 v[64:65], v[64:65], v[230:231] op_sel_hi:[1,0]
	v_pk_mul_f32 v[66:67], v[66:67], v[230:231] op_sel_hi:[1,0]
	s_waitcnt lgkmcnt(3)
	v_pk_mul_f32 v[64:65], v[72:73], v[64:65]
	v_lshlrev_b32_e32 v72, 16, v177
	v_and_b32_e32 v73, 0xffff0000, v177
	v_pk_mul_f32 v[66:67], v[74:75], v[66:67]
	v_pk_mul_f32 v[74:75], v[88:89], v[230:231] op_sel_hi:[1,0]
	v_pk_mul_f32 v[66:67], v[66:67], v[72:73]
	v_lshlrev_b32_e32 v72, 16, v178
	v_and_b32_e32 v73, 0xffff0000, v178
	s_waitcnt lgkmcnt(2)
	v_pk_mul_f32 v[74:75], v[76:77], v[74:75]
	v_pk_mul_f32 v[76:77], v[90:91], v[230:231] op_sel_hi:[1,0]
	v_pk_mul_f32 v[72:73], v[74:75], v[72:73]
	v_lshlrev_b32_e32 v74, 16, v179
	v_and_b32_e32 v75, 0xffff0000, v179
	v_pk_mul_f32 v[76:77], v[78:79], v[76:77]
	v_pk_mul_f32 v[64:65], v[64:65], v[232:233]
	v_pk_mul_f32 v[74:75], v[76:77], v[74:75]
	v_add_co_u32_e32 v76, vcc, s2, v200
	v_cvt_pk_bf16_f32 v64, v64, v65
	v_cvt_pk_bf16_f32 v65, v66, v67
	v_cvt_pk_bf16_f32 v66, v72, v73
	v_cvt_pk_bf16_f32 v67, v74, v75
	v_addc_co_u32_e32 v77, vcc, 0, v201, vcc
	global_store_dwordx4 v[76:77], v[64:67], off offset:2048
	v_pk_mul_f32 v[72:73], v[94:95], v[230:231] op_sel_hi:[1,0]
	v_pk_mul_f32 v[74:75], v[192:193], v[230:231] op_sel_hi:[1,0]
	v_pk_mul_f32 v[66:67], v[92:93], v[230:231] op_sel_hi:[1,0]
	s_waitcnt vmcnt(9)
; #define LAS __attribute__((address_space(3)))
; __device__ __forceinline__ unsigned cvt_pk_bf16(float lo, float hi) { const bf16x2_t r = __builtin_convertvector((f32x2_t){lo, hi}, bf16x2_t); return __builtin_bit_cast(unsigned, r); }
; __device__ __forceinline__ float bf_lo(unsigned w) { return __uint_as_float(w << 16); }
; __device__ __forceinline__ float bf_hi(unsigned w) { return __uint_as_float(w & 0xffff0000u); }
; __device__ __forceinline__ void gla_unit(LAS unsigned char* lds, const unsigned char* ws, const float* g_onorm, const int b, const int h, const int wv) {
;     ...
;             bf16_t* mp = mix + (t0 + t) * DM + 1024 + h * 256 + 32 * g8;
; #pragma unroll
;             for (int x = 0; x < 4; ++x) {
;                 const u32x4 og = ogr[x];
;                 const f32x4 g0 = *(const LAS f32x4*)&gon[32 * g8 + 8 * x], g1 = *(const LAS f32x4*)&gon[32 * g8 + 8 * x + 4];
;                 const float gg2[8] = {g0[0], g0[1], g0[2], g0[3], g1[0], g1[1], g1[2], g1[3]};
;                 float res[8];
; #pragma unroll
;                 for (int y = 0; y < 4; ++y) { const float a0 = bf_lo(og[y]), a1 = bf_hi(og[y]);
;                     res[2 * y] = ov[8 * x + 2 * y] * rstd * gg2[2 * y] * a0;
;                     res[2 * y + 1] = ov[8 * x + 2 * y + 1] * rstd * gg2[2 * y + 1] * a1; }
;                 u32x4 wv4; wv4[0] = cvt_pk_bf16(res[0], res[1]); wv4[1] = cvt_pk_bf16(res[2], res[3]); wv4[2] = cvt_pk_bf16(res[4], res[5]); wv4[3] = cvt_pk_bf16(res[6], res[7]);
;                 *(u32x4*)(mp + 8 * x) = wv4;
;             }
	v_lshlrev_b32_e32 v64, 16, v172
	v_and_b32_e32 v65, 0xffff0000, v172
	s_waitcnt lgkmcnt(1)
	v_pk_mul_f32 v[66:67], v[80:81], v[66:67]
	v_pk_mul_f32 v[72:73], v[82:83], v[72:73]
	v_pk_mul_f32 v[64:65], v[66:67], v[64:65]
	v_lshlrev_b32_e32 v66, 16, v173
	v_and_b32_e32 v67, 0xffff0000, v173
	v_pk_mul_f32 v[66:67], v[72:73], v[66:67]
	v_lshlrev_b32_e32 v72, 16, v174
	v_and_b32_e32 v73, 0xffff0000, v174
	s_waitcnt lgkmcnt(0)
	v_pk_mul_f32 v[74:75], v[84:85], v[74:75]
	v_pk_mul_f32 v[78:79], v[194:195], v[230:231] op_sel_hi:[1,0]
	v_pk_mul_f32 v[72:73], v[74:75], v[72:73]
	v_lshlrev_b32_e32 v74, 16, v175
	v_and_b32_e32 v75, 0xffff0000, v175
	v_pk_mul_f32 v[78:79], v[86:87], v[78:79]
	v_cvt_pk_bf16_f32 v64, v64, v65
	v_pk_mul_f32 v[74:75], v[78:79], v[74:75]
	v_cvt_pk_bf16_f32 v65, v66, v67
	v_cvt_pk_bf16_f32 v66, v72, v73
	v_cvt_pk_bf16_f32 v67, v74, v75
	global_store_dwordx4 v[76:77], v[64:67], off offset:2064
	ds_read_b128 v[64:67], v208 offset:64
	ds_read_b128 v[72:75], v208 offset:80
	v_pk_mul_f32 v[68:69], v[68:69], v[230:231] op_sel_hi:[1,0]
	v_pk_mul_f32 v[70:71], v[70:71], v[230:231] op_sel_hi:[1,0]
	v_lshlrev_b32_e32 v78, 16, v168
	s_waitcnt lgkmcnt(1)
	v_pk_mul_f32 v[64:65], v[64:65], v[68:69]
	v_lshlrev_b32_e32 v68, 16, v169
	v_and_b32_e32 v69, 0xffff0000, v169
	v_pk_mul_f32 v[66:67], v[66:67], v[70:71]
	v_pk_mul_f32 v[70:71], v[196:197], v[230:231] op_sel_hi:[1,0]
	v_pk_mul_f32 v[66:67], v[66:67], v[68:69]
	v_lshlrev_b32_e32 v68, 16, v170
	v_and_b32_e32 v69, 0xffff0000, v170
	s_waitcnt lgkmcnt(0)
	v_pk_mul_f32 v[70:71], v[72:73], v[70:71]
	v_pk_mul_f32 v[72:73], v[198:199], v[230:231] op_sel_hi:[1,0]
	v_and_b32_e32 v79, 0xffff0000, v168
	v_pk_mul_f32 v[68:69], v[70:71], v[68:69]
	v_lshlrev_b32_e32 v70, 16, v171
	v_and_b32_e32 v71, 0xffff0000, v171
	v_pk_mul_f32 v[72:73], v[74:75], v[72:73]
	v_pk_mul_f32 v[64:65], v[64:65], v[78:79]
	v_pk_mul_f32 v[70:71], v[72:73], v[70:71]
	v_cvt_pk_bf16_f32 v64, v64, v65
	v_cvt_pk_bf16_f32 v65, v66, v67
	v_cvt_pk_bf16_f32 v66, v68, v69
	v_cvt_pk_bf16_f32 v67, v70, v71
	global_store_dwordx4 v[76:77], v[64:67], off offset:2080
	ds_read_b128 v[64:67], v208 offset:96
	ds_read_b128 v[68:71], v208 offset:112
	v_pk_mul_f32 v[74:75], v[222:223], v[230:231] op_sel_hi:[1,0]
	v_lshlrev_b32_e32 v72, 16, v164
	v_and_b32_e32 v73, 0xffff0000, v164
	s_waitcnt lgkmcnt(1)
	v_pk_mul_f32 v[64:65], v[74:75], v[64:65]
	v_pk_mul_f32 v[74:75], v[224:225], v[230:231] op_sel_hi:[1,0]
	v_pk_mul_f32 v[64:65], v[64:65], v[72:73]
	v_lshlrev_b32_e32 v72, 16, v165
	v_and_b32_e32 v73, 0xffff0000, v165
	v_pk_mul_f32 v[66:67], v[74:75], v[66:67]
	v_pk_mul_f32 v[74:75], v[226:227], v[230:231] op_sel_hi:[1,0]
	v_pk_mul_f32 v[66:67], v[66:67], v[72:73]
	v_lshlrev_b32_e32 v72, 16, v166
	v_and_b32_e32 v73, 0xffff0000, v166
	s_waitcnt lgkmcnt(0)
	v_pk_mul_f32 v[68:69], v[74:75], v[68:69]
	v_pk_mul_f32 v[74:75], v[228:229], v[230:231] op_sel_hi:[1,0]
	v_pk_mul_f32 v[68:69], v[68:69], v[72:73]
	v_lshlrev_b32_e32 v72, 16, v167
	v_and_b32_e32 v73, 0xffff0000, v167
	v_pk_mul_f32 v[70:71], v[74:75], v[70:71]
	s_mov_b64 s[2:3], 0x40000
	v_pk_mul_f32 v[70:71], v[70:71], v[72:73]
	v_lshl_add_u64 v[182:183], v[182:183], 0, s[2:3]
	s_mov_b64 s[2:3], 0x8000
	v_cvt_pk_bf16_f32 v64, v64, v65
	v_cvt_pk_bf16_f32 v65, v66, v67
	v_cvt_pk_bf16_f32 v66, v68, v69
	v_cvt_pk_bf16_f32 v67, v70, v71
	v_lshl_add_u64 v[186:187], v[186:187], 0, s[2:3]
	global_store_dwordx4 v[76:77], v[64:67], off offset:2096
	s_cbranch_scc0 .LBB0_655

; #define LAS __attribute__((address_space(3)))
; __device__ __forceinline__ void gla_unit(LAS unsigned char* lds, const unsigned char* ws, const float* g_onorm, const int b, const int h, const int wv) {
;     ...
;         f32x16 O[2];
; #pragma unroll
;         for (int tt = 0; tt < 2; ++tt)
; #pragma unroll
;             for (int r = 0; r < 16; ++r) O[tt][r] = 0.f;
; #pragma unroll
;         for (int et = 0; et < 4; ++et)
; #pragma unroll
;             for (int s2 = 0; s2 < 2; ++s2) {
;                 const bf16x8 sb = pack8(S[et], s2);
; #pragma unroll
;                 for (int tt = 0; tt < 2; ++tt) {
;                     const bf16x8 aq = ld2x64(qb8 + 32 * tt * QS + (32 * et + 16 * s2) * 2);
;                     O[tt] = __builtin_amdgcn_mfma_f32_32x32x16_bf16(aq, sb, O[tt], 0, 0, 0);
;                 }
;             }
;         __syncthreads();
; #pragma unroll
;         for (int pr = 0; pr < 3; ++pr) {
;             const int st = (pr == 2) ? 1 : 0, tt = (pr == 0) ? 0 : 1;
; #pragma unroll
;             for (int s2 = 0; s2 < 2; ++s2) {
;                 const bf16x8 ax = *(const LAS bf16x8*)(frb + (pr * 2 + s2) * 1024);
;                 const LAS unsigned char* vp = vP + (32 * st + 16 * s2) * VS;
;                 const bf16x8 bv = tr8(vp, vp + 8 * VS);
;                 O[tt] = __builtin_amdgcn_mfma_f32_32x32x16_bf16(ax, bv, O[tt], 0, 0, 0);
;             }
;         }
;         __builtin_amdgcn_sched_barrier(0);
; #pragma unroll
;         for (int tt = 0; tt < 2; ++tt)
; #pragma unroll
;             for (int r = 0; r < 16; ++r) ob[(32 * tt + (r & 3) + 8 * (r >> 2)) * OS] = O[tt][r];
;         __builtin_amdgcn_sched_barrier(0);
; #pragma unroll
;         for (int et = 0; et < 4; ++et)
; #pragma unroll
;             for (int rg = 0; rg < 4; ++rg) { const f32x4 dl = *(const LAS f32x4*)&decb[32 * et + 8 * rg];
.LBB0_646:
	v_add_u32_e32 v222, v203, v202
	ds_read2_b64 v[64:67], v222 offset1:2
	v_cvt_pk_bf16_f32 v68, v32, v33
	v_cvt_pk_bf16_f32 v69, v34, v35
	v_cvt_pk_bf16_f32 v70, v36, v37
	v_cvt_pk_bf16_f32 v71, v38, v39
	v_add_u32_e32 v223, 0x2000, v222
	ds_read2_b64 v[228:231], v222 offset0:4 offset1:6
	v_cvt_pk_bf16_f32 v232, v40, v41
	v_cvt_pk_bf16_f32 v233, v42, v43
	s_waitcnt lgkmcnt(1)
	v_mfma_f32_32x32x16_bf16 v[80:95], v[64:67], v[68:71], 0
	ds_read2_b64 v[64:67], v223 offset0:64 offset1:66
	v_cvt_pk_bf16_f32 v234, v44, v45
	v_cvt_pk_bf16_f32 v235, v46, v47
	s_waitcnt lgkmcnt(1)
	s_nop 0
	v_mfma_f32_32x32x16_bf16 v[80:95], v[228:231], v[232:235], v[80:95]
	ds_read2_b64 v[228:231], v223 offset0:68 offset1:70
	s_waitcnt lgkmcnt(1)
	v_mfma_f32_32x32x16_bf16 v[64:79], v[64:67], v[68:71], 0
	s_waitcnt lgkmcnt(0)
	v_mfma_f32_32x32x16_bf16 v[64:79], v[228:231], v[232:235], v[64:79]
	ds_read2_b64 v[228:231], v222 offset0:8 offset1:10
	ds_read2_b64 v[236:239], v223 offset0:72 offset1:74
	ds_read2_b64 v[240:243], v222 offset0:12 offset1:14
	v_cvt_pk_bf16_f32 v232, v16, v17
	v_cvt_pk_bf16_f32 v233, v18, v19
	v_cvt_pk_bf16_f32 v234, v20, v21
	v_cvt_pk_bf16_f32 v235, v22, v23
	s_waitcnt lgkmcnt(2)
	s_nop 0
	v_mfma_f32_32x32x16_bf16 v[80:95], v[228:231], v[232:235], v[80:95]
	ds_read2_b64 v[248:251], v223 offset0:76 offset1:78
	s_waitcnt lgkmcnt(2)
	v_mfma_f32_32x32x16_bf16 v[64:79], v[236:239], v[232:235], v[64:79]
	ds_read2_b64 v[228:231], v222 offset0:16 offset1:18
	v_cvt_pk_bf16_f32 v232, v24, v25
	v_cvt_pk_bf16_f32 v233, v26, v27
	v_cvt_pk_bf16_f32 v234, v28, v29
	v_cvt_pk_bf16_f32 v235, v30, v31
	s_waitcnt lgkmcnt(2)
	s_nop 0
	v_mfma_f32_32x32x16_bf16 v[80:95], v[240:243], v[232:235], v[80:95]
	ds_read2_b64 v[236:239], v223 offset0:80 offset1:82
	s_waitcnt lgkmcnt(2)
	v_mfma_f32_32x32x16_bf16 v[64:79], v[248:251], v[232:235], v[64:79]
	ds_read2_b64 v[240:243], v222 offset0:20 offset1:22
	v_cvt_pk_bf16_f32 v232, v48, v49
	v_cvt_pk_bf16_f32 v233, v50, v51
	v_cvt_pk_bf16_f32 v234, v52, v53
	v_cvt_pk_bf16_f32 v235, v54, v55
	s_waitcnt lgkmcnt(2)
	s_nop 0
	v_mfma_f32_32x32x16_bf16 v[80:95], v[228:231], v[232:235], v[80:95]
	ds_read2_b64 v[248:251], v223 offset0:84 offset1:86
	s_waitcnt lgkmcnt(2)
	v_mfma_f32_32x32x16_bf16 v[64:79], v[236:239], v[232:235], v[64:79]
	ds_read2_b64 v[228:231], v222 offset0:24 offset1:26
	v_cvt_pk_bf16_f32 v232, v56, v57
	v_cvt_pk_bf16_f32 v233, v58, v59
	v_cvt_pk_bf16_f32 v234, v60, v61
	v_cvt_pk_bf16_f32 v235, v62, v63
	s_waitcnt lgkmcnt(2)
	s_nop 0
	v_mfma_f32_32x32x16_bf16 v[80:95], v[240:243], v[232:235], v[80:95]
	ds_read2_b64 v[236:239], v223 offset0:88 offset1:90
	s_waitcnt lgkmcnt(2)
	v_mfma_f32_32x32x16_bf16 v[64:79], v[248:251], v[232:235], v[64:79]
	ds_read2_b64 v[240:243], v222 offset0:28 offset1:30
	v_cvt_pk_bf16_f32 v232, v0, v1
	v_cvt_pk_bf16_f32 v233, v2, v3
	v_cvt_pk_bf16_f32 v234, v4, v5
	v_cvt_pk_bf16_f32 v235, v6, v7
	s_waitcnt lgkmcnt(2)
	s_nop 0
	v_mfma_f32_32x32x16_bf16 v[80:95], v[228:231], v[232:235], v[80:95]
	ds_read2_b64 v[248:251], v223 offset0:92 offset1:94
	s_waitcnt lgkmcnt(2)
	v_mfma_f32_32x32x16_bf16 v[64:79], v[236:239], v[232:235], v[64:79]
	v_cvt_pk_bf16_f32 v232, v8, v9
	v_cvt_pk_bf16_f32 v233, v10, v11
	v_cvt_pk_bf16_f32 v234, v12, v13
	v_cvt_pk_bf16_f32 v235, v14, v15
	s_waitcnt lgkmcnt(1)
	s_nop 0
	v_mfma_f32_32x32x16_bf16 v[80:95], v[240:243], v[232:235], v[80:95]
	s_waitcnt lgkmcnt(0)
	s_barrier
	v_mfma_f32_32x32x16_bf16 v[64:79], v[248:251], v[232:235], v[64:79]
	ds_read_b128 v[228:231], v206
	ds_read_b64_tr_b16 v[232:233], v218
	ds_read_b64_tr_b16 v[234:235], v218 offset:4608
	ds_read_b128 v[236:239], v206 offset:1024
	ds_read_b64_tr_b16 v[240:241], v218 offset:9216
	ds_read_b64_tr_b16 v[242:243], v218 offset:13824
	s_waitcnt lgkmcnt(3)
	v_mfma_f32_32x32x16_bf16 v[80:95], v[228:231], v[232:235], v[80:95]
	s_waitcnt lgkmcnt(0)
	v_mfma_f32_32x32x16_bf16 v[80:95], v[236:239], v[240:243], v[80:95]
	ds_read_b128 v[228:231], v206 offset:2048
	ds_read_b128 v[236:239], v206 offset:3072
	s_waitcnt lgkmcnt(1)
	v_mfma_f32_32x32x16_bf16 v[64:79], v[228:231], v[232:235], v[64:79]
	s_waitcnt lgkmcnt(0)
	v_mfma_f32_32x32x16_bf16 v[64:79], v[236:239], v[240:243], v[64:79]
	ds_read_b128 v[228:231], v206 offset:4096
	ds_read_b64_tr_b16 v[232:233], v218 offset:18432
	ds_read_b64_tr_b16 v[234:235], v218 offset:23040
	ds_read_b128 v[236:239], v206 offset:5120
	ds_read_b64_tr_b16 v[240:241], v218 offset:27648
	ds_read_b64_tr_b16 v[242:243], v218 offset:32256
	s_waitcnt lgkmcnt(3)
	v_mfma_f32_32x32x16_bf16 v[64:79], v[228:231], v[232:235], v[64:79]
	s_waitcnt lgkmcnt(0)
	v_mfma_f32_32x32x16_bf16 v[64:79], v[236:239], v[240:243], v[64:79]
	ds_write_b32 v207, v80
	ds_write_b32 v207, v81 offset:1040
	ds_write_b32 v207, v82 offset:2080
	ds_write_b32 v207, v83 offset:3120
	ds_write_b32 v207, v84 offset:8320
	ds_write_b32 v207, v85 offset:9360
	ds_write_b32 v207, v86 offset:10400
	ds_write_b32 v207, v87 offset:11440
	ds_write_b32 v207, v88 offset:16640
	ds_write_b32 v207, v89 offset:17680
	ds_write_b32 v207, v90 offset:18720
	ds_write_b32 v207, v91 offset:19760
	ds_write_b32 v207, v92 offset:24960
	ds_write_b32 v207, v93 offset:26000
	ds_write_b32 v207, v94 offset:27040
	ds_write_b32 v207, v95 offset:28080
	ds_write_b32 v207, v64 offset:33280
	ds_write_b32 v207, v65 offset:34320
	ds_write_b32 v207, v66 offset:35360
	ds_write_b32 v207, v67 offset:36400
	ds_write_b32 v207, v68 offset:41600
	ds_write_b32 v207, v69 offset:42640
	ds_write_b32 v207, v70 offset:43680
	ds_write_b32 v207, v71 offset:44720
	ds_write_b32 v207, v72 offset:49920
	ds_write_b32 v207, v73 offset:50960
	ds_write_b32 v207, v74 offset:52000
	ds_write_b32 v207, v75 offset:53040
	ds_write_b32 v207, v76 offset:58240
	ds_write_b32 v207, v77 offset:59280
	ds_write_b32 v207, v78 offset:60320
	ds_write_b32 v207, v79 offset:61360
	ds_read_b128 v[64:67], v205
	ds_read_b128 v[68:71], v205 offset:32
	ds_read_b128 v[72:75], v205 offset:64
	ds_read_b128 v[76:79], v205 offset:96
	s_waitcnt vmcnt(11)
; #define LAS __attribute__((address_space(3)))
; __device__ __forceinline__ void gla_unit(LAS unsigned char* lds, const unsigned char* ws, const float* g_onorm, const int b, const int h, const int wv) {
;     ...
; #pragma unroll
;         for (int et = 0; et < 4; ++et)
; #pragma unroll
;             for (int rg = 0; rg < 4; ++rg) { const f32x4 dl = *(const LAS f32x4*)&decb[32 * et + 8 * rg];
; #pragma unroll
;                 for (int x = 0; x < 4; ++x) S[et][4 * rg + x] *= dl[x]; }
; #pragma unroll
;         for (int ks = 0; ks < 4; ++ks) {
;             const LAS unsigned char* vp = vN + 16 * ks * VS;
;             const bf16x8 bv = tr8(vp, vp + 4 * VS);
; #pragma unroll
;             for (int et = 0; et < 4; ++et) {
;                 const LAS unsigned char* kp = keN + 32 * et * 2 + 16 * ks * ES;
;                 const bf16x8 ak = tr8(kp, kp + 4 * ES);
;                 S[et] = __builtin_amdgcn_mfma_f32_32x32x16_bf16(ak, bv, S[et], 0, 0, 0);
;             }
;         }
	v_lshlrev_b32_e32 v246, 16, v176
	s_waitcnt lgkmcnt(3)
	v_mul_f32_e32 v34, v34, v66
	v_mul_f32_e32 v35, v35, v67
	s_waitcnt lgkmcnt(2)
	v_mul_f32_e32 v38, v38, v70
	v_mul_f32_e32 v39, v39, v71
	s_waitcnt lgkmcnt(1)
	v_mul_f32_e32 v42, v42, v74
	v_mul_f32_e32 v43, v43, v75
	s_waitcnt lgkmcnt(0)
	v_mul_f32_e32 v46, v46, v78
	v_mul_f32_e32 v47, v47, v79
	v_mul_f32_e32 v44, v44, v76
	v_mul_f32_e32 v45, v45, v77
	v_mul_f32_e32 v40, v40, v72
	v_mul_f32_e32 v41, v41, v73
	v_mul_f32_e32 v36, v36, v68
	v_mul_f32_e32 v37, v37, v69
	v_mul_f32_e32 v32, v32, v64
	v_mul_f32_e32 v33, v33, v65
	ds_read_b128 v[64:67], v205 offset:128
	ds_read_b128 v[68:71], v205 offset:160
	ds_read_b128 v[72:75], v205 offset:192
	ds_read_b128 v[76:79], v205 offset:224
	v_and_b32_e32 v247, 0xffff0000, v176
	s_waitcnt lgkmcnt(3)
	v_mul_f32_e32 v18, v18, v66
	v_mul_f32_e32 v19, v19, v67
	s_waitcnt lgkmcnt(2)
	v_mul_f32_e32 v22, v22, v70
	v_mul_f32_e32 v23, v23, v71
	s_waitcnt lgkmcnt(1)
	v_mul_f32_e32 v26, v26, v74
	v_mul_f32_e32 v27, v27, v75
	s_waitcnt lgkmcnt(0)
	v_mul_f32_e32 v30, v30, v78
	v_mul_f32_e32 v31, v31, v79
	v_mul_f32_e32 v28, v28, v76
	v_mul_f32_e32 v29, v29, v77
	v_mul_f32_e32 v24, v24, v72
	v_mul_f32_e32 v25, v25, v73
	v_mul_f32_e32 v20, v20, v68
	v_mul_f32_e32 v21, v21, v69
	v_mul_f32_e32 v16, v16, v64
	v_mul_f32_e32 v17, v17, v65
	ds_read_b128 v[64:67], v205 offset:256
	ds_read_b128 v[68:71], v205 offset:288
	ds_read_b128 v[72:75], v205 offset:320
	ds_read_b128 v[76:79], v205 offset:352
	v_lshlrev_b32_e32 v176, 16, v177
	s_waitcnt lgkmcnt(3)
	v_mul_f32_e32 v50, v50, v66
	v_mul_f32_e32 v51, v51, v67
	s_waitcnt lgkmcnt(2)
	v_mul_f32_e32 v54, v54, v70
	v_mul_f32_e32 v55, v55, v71
	s_waitcnt lgkmcnt(1)
	v_mul_f32_e32 v58, v58, v74
	v_mul_f32_e32 v59, v59, v75
	s_waitcnt lgkmcnt(0)
	v_mul_f32_e32 v62, v62, v78
	v_mul_f32_e32 v63, v63, v79
	v_mul_f32_e32 v60, v60, v76
	v_mul_f32_e32 v61, v61, v77
	v_mul_f32_e32 v56, v56, v72
	v_mul_f32_e32 v57, v57, v73
	v_mul_f32_e32 v52, v52, v68
	v_mul_f32_e32 v53, v53, v69
	v_mul_f32_e32 v48, v48, v64
	v_mul_f32_e32 v49, v49, v65
	ds_read_b128 v[64:67], v205 offset:384
	ds_read_b128 v[68:71], v205 offset:416
	ds_read_b128 v[72:75], v205 offset:448
	ds_read_b128 v[76:79], v205 offset:480
	v_and_b32_e32 v177, 0xffff0000, v177
	s_waitcnt lgkmcnt(3)
	v_mul_f32_e32 v2, v2, v66
	v_mul_f32_e32 v3, v3, v67
	s_waitcnt lgkmcnt(2)
	v_mul_f32_e32 v6, v6, v70
	v_mul_f32_e32 v7, v7, v71
	v_mul_f32_e32 v4, v4, v68
	v_mul_f32_e32 v5, v5, v69
	v_mul_f32_e32 v0, v0, v64
	v_mul_f32_e32 v1, v1, v65
	ds_read_b64_tr_b16 v[64:65], v219
	ds_read_b64_tr_b16 v[66:67], v219 offset:2304
	ds_read_b64_tr_b16 v[68:69], v220
	ds_read_b64_tr_b16 v[70:71], v220 offset:1280
	ds_read_b64_tr_b16 v[80:81], v220 offset:64
	ds_read_b64_tr_b16 v[82:83], v220 offset:1344
	ds_read_b64_tr_b16 v[84:85], v220 offset:128
	ds_read_b64_tr_b16 v[86:87], v220 offset:1408
	ds_read_b64_tr_b16 v[88:89], v220 offset:192
	ds_read_b64_tr_b16 v[90:91], v220 offset:1472
	ds_read_b64_tr_b16 v[92:93], v219 offset:9216
	ds_read_b64_tr_b16 v[94:95], v219 offset:11520
	s_waitcnt lgkmcnt(8)
	v_mfma_f32_32x32x16_bf16 v[32:47], v[68:71], v[64:67], v[32:47]
	ds_read_b64_tr_b16 v[68:69], v220 offset:5120
	ds_read_b64_tr_b16 v[70:71], v220 offset:6400
	v_mul_f32_e64 v14, v14, v78
	v_mul_f32_e64 v15, v15, v79
	v_mul_f32_e64 v10, v10, v74
	v_mul_f32_e64 v11, v11, v75
	v_mul_f32_e32 v12, v12, v76
	v_mul_f32_e32 v13, v13, v77
	v_mul_f32_e32 v8, v8, v72
	v_mul_f32_e32 v9, v9, v73
	s_waitcnt lgkmcnt(8)
	v_mfma_f32_32x32x16_bf16 v[16:31], v[80:83], v[64:67], v[16:31]
	ds_read_b64_tr_b16 v[80:81], v220 offset:5184
	ds_read_b64_tr_b16 v[82:83], v220 offset:6464
	s_waitcnt lgkmcnt(8)
	v_mfma_f32_32x32x16_bf16 v[48:63], v[84:87], v[64:67], v[48:63]
	ds_read_b64_tr_b16 v[84:85], v220 offset:5248
	ds_read_b64_tr_b16 v[86:87], v220 offset:6528
	s_waitcnt lgkmcnt(8)
	v_mfma_f32_32x32x16_bf16 v[0:15], v[88:91], v[64:67], v[0:15]
	ds_read_b64_tr_b16 v[88:89], v220 offset:5312
	ds_read_b64_tr_b16 v[90:91], v220 offset:6592
	ds_read_b64_tr_b16 v[64:65], v219 offset:18432
	ds_read_b64_tr_b16 v[66:67], v219 offset:20736
	s_waitcnt lgkmcnt(8)
	v_mfma_f32_32x32x16_bf16 v[32:47], v[68:71], v[92:95], v[32:47]
	ds_read_b64_tr_b16 v[68:69], v220 offset:10240
	ds_read_b64_tr_b16 v[70:71], v220 offset:11520
	s_waitcnt lgkmcnt(8)
	v_mfma_f32_32x32x16_bf16 v[16:31], v[80:83], v[92:95], v[16:31]
	ds_read_b64_tr_b16 v[80:81], v220 offset:10304
	ds_read_b64_tr_b16 v[82:83], v220 offset:11584
	s_waitcnt lgkmcnt(8)
	v_mfma_f32_32x32x16_bf16 v[48:63], v[84:87], v[92:95], v[48:63]
	ds_read_b64_tr_b16 v[84:85], v220 offset:10368
	ds_read_b64_tr_b16 v[86:87], v220 offset:11648
	s_waitcnt lgkmcnt(8)
	v_mfma_f32_32x32x16_bf16 v[0:15], v[88:91], v[92:95], v[0:15]
	ds_read_b64_tr_b16 v[88:89], v220 offset:10432
	ds_read_b64_tr_b16 v[90:91], v220 offset:11712
	ds_read_b64_tr_b16 v[92:93], v219 offset:27648
	ds_read_b64_tr_b16 v[94:95], v219 offset:29952
	s_waitcnt lgkmcnt(8)
	v_mfma_f32_32x32x16_bf16 v[32:47], v[68:71], v[64:67], v[32:47]
	ds_read_b64_tr_b16 v[68:69], v220 offset:15360
	ds_read_b64_tr_b16 v[70:71], v220 offset:16640
	s_waitcnt lgkmcnt(8)
	v_mfma_f32_32x32x16_bf16 v[16:31], v[80:83], v[64:67], v[16:31]
	ds_read_b64_tr_b16 v[80:81], v220 offset:15424
	ds_read_b64_tr_b16 v[82:83], v220 offset:16704
	s_waitcnt lgkmcnt(8)
	v_mfma_f32_32x32x16_bf16 v[48:63], v[84:87], v[64:67], v[48:63]
	ds_read_b64_tr_b16 v[84:85], v220 offset:15488
	ds_read_b64_tr_b16 v[86:87], v220 offset:16768
	s_waitcnt lgkmcnt(8)
	v_mfma_f32_32x32x16_bf16 v[0:15], v[88:91], v[64:67], v[0:15]
	ds_read_b64_tr_b16 v[88:89], v220 offset:15552
	ds_read_b64_tr_b16 v[90:91], v220 offset:16832
	s_waitcnt lgkmcnt(6)
	v_mfma_f32_32x32x16_bf16 v[32:47], v[68:71], v[92:95], v[32:47]
	s_waitcnt lgkmcnt(4)
	v_mfma_f32_32x32x16_bf16 v[16:31], v[80:83], v[92:95], v[16:31]
	s_waitcnt lgkmcnt(2)
	v_mfma_f32_32x32x16_bf16 v[48:63], v[84:87], v[92:95], v[48:63]
	s_waitcnt lgkmcnt(0)
	s_barrier
; #define LAS __attribute__((address_space(3)))
; __device__ __forceinline__ unsigned cvt_pk_bf16(float lo, float hi) { const bf16x2_t r = __builtin_convertvector((f32x2_t){lo, hi}, bf16x2_t); return __builtin_bit_cast(unsigned, r); }
; __device__ __forceinline__ float bf_lo(unsigned w) { return __uint_as_float(w << 16); }
; __device__ __forceinline__ float bf_hi(unsigned w) { return __uint_as_float(w & 0xffff0000u); }
; __device__ __forceinline__ void gla_unit(LAS unsigned char* lds, const unsigned char* ws, const float* g_onorm, const int b, const int h, const int wv) {
;     ...
;         {
;             const int t = tid >> 3, g8 = tid & 7;
;             float ov[32]; float ss = 0.f;
; #pragma unroll
;             for (int x = 0; x < 8; ++x) { const f32x4 v = *(const LAS f32x4*)&obuf[t * OS + 32 * g8 + 4 * x]; ov[4 * x] = v[0]; ov[4 * x + 1] = v[1]; ov[4 * x + 2] = v[2]; ov[4 * x + 3] = v[3];
;                 ss += v[0] * v[0] + v[1] * v[1] + v[2] * v[2] + v[3] * v[3]; }
;             ss += __builtin_bit_cast(float, __builtin_amdgcn_ds_swizzle(__builtin_bit_cast(int, ss), (1 << 10) | 0x1F)); ss += __builtin_bit_cast(float, __builtin_amdgcn_ds_swizzle(__builtin_bit_cast(int, ss), (2 << 10) | 0x1F));
;             ss += __builtin_bit_cast(float, __builtin_amdgcn_ds_swizzle(__builtin_bit_cast(int, ss), (4 << 10) | 0x1F));
;             const float rstd = __builtin_amdgcn_rsqf(ss * (1.0f / 256.0f) + EPSV);
;             bf16_t* mp = mix + (t0 + t) * DM + 1024 + h * 256 + 32 * g8;
; #pragma unroll
;             for (int x = 0; x < 4; ++x) {
;                 const u32x4 og = ogr[x];
;                 const f32x4 g0 = *(const LAS f32x4*)&gon[32 * g8 + 8 * x], g1 = *(const LAS f32x4*)&gon[32 * g8 + 8 * x + 4];
;                 const float gg2[8] = {g0[0], g0[1], g0[2], g0[3], g1[0], g1[1], g1[2], g1[3]};
;                 float res[8];
; #pragma unroll
;                 for (int y = 0; y < 4; ++y) { const float a0 = bf_lo(og[y]), a1 = bf_hi(og[y]);
;                     res[2 * y] = ov[8 * x + 2 * y] * rstd * gg2[2 * y] * a0;
;                     res[2 * y + 1] = ov[8 * x + 2 * y + 1] * rstd * gg2[2 * y + 1] * a1; }
;                 u32x4 wv4; wv4[0] = cvt_pk_bf16(res[0], res[1]); wv4[1] = cvt_pk_bf16(res[2], res[3]); wv4[2] = cvt_pk_bf16(res[4], res[5]); wv4[3] = cvt_pk_bf16(res[6], res[7]);
;                 *(u32x4*)(mp + 8 * x) = wv4;
;             }
	v_mfma_f32_32x32x16_bf16 v[0:15], v[88:91], v[92:95], v[0:15]
	ds_read_b128 v[64:67], v221
	ds_read_b128 v[68:71], v221 offset:16
	ds_read_b128 v[72:75], v221 offset:32
	ds_read_b128 v[76:79], v221 offset:48
	s_waitcnt lgkmcnt(3)
	v_mul_f32_e32 v80, v65, v65
	s_waitcnt lgkmcnt(2)
	v_mul_f32_e32 v81, v69, v69
	v_fmac_f32_e32 v80, v64, v64
	v_fmac_f32_e32 v81, v68, v68
	v_fmac_f32_e32 v80, v66, v66
	v_fmac_f32_e32 v81, v70, v70
	v_fmac_f32_e32 v80, v67, v67
	v_fmac_f32_e32 v81, v71, v71
	s_waitcnt lgkmcnt(1)
	v_mov_b32_e32 v82, v73
	s_waitcnt lgkmcnt(0)
	v_mov_b32_e32 v83, v77
	v_add_f32_e32 v84, v80, v81
	v_mov_b32_e32 v80, v72
	v_mov_b32_e32 v81, v76
	v_pk_mul_f32 v[82:83], v[82:83], v[82:83]
	s_nop 0
	v_pk_fma_f32 v[80:81], v[80:81], v[80:81], v[82:83]
	v_mov_b32_e32 v82, v74
	v_mov_b32_e32 v83, v78
	v_pk_fma_f32 v[80:81], v[82:83], v[82:83], v[80:81]
	v_mov_b32_e32 v82, v75
	v_mov_b32_e32 v83, v79
	v_pk_fma_f32 v[80:81], v[82:83], v[82:83], v[80:81]
	s_nop 0
	v_add_f32_e32 v80, v84, v80
	v_add_f32_e32 v92, v80, v81
	ds_read_b128 v[80:83], v221 offset:64
	ds_read_b128 v[84:87], v221 offset:80
	s_waitcnt lgkmcnt(1)
	v_mov_b32_e32 v90, v81
	s_waitcnt lgkmcnt(0)
	v_mov_b32_e32 v91, v85
	v_mov_b32_e32 v88, v80
	v_mov_b32_e32 v89, v84
	v_pk_mul_f32 v[90:91], v[90:91], v[90:91]
	s_nop 0
	v_pk_fma_f32 v[88:89], v[88:89], v[88:89], v[90:91]
	v_mov_b32_e32 v90, v82
	v_mov_b32_e32 v91, v86
	v_pk_fma_f32 v[88:89], v[90:91], v[90:91], v[88:89]
	v_mov_b32_e32 v90, v83
	v_mov_b32_e32 v91, v87
	v_pk_fma_f32 v[88:89], v[90:91], v[90:91], v[88:89]
	s_nop 0
	v_add_f32_e32 v88, v92, v88
	v_add_f32_e32 v227, v88, v89
	ds_read_b128 v[88:91], v221 offset:96
	ds_read_b128 v[92:95], v221 offset:112
	s_waitcnt lgkmcnt(1)
	v_mov_b32_e32 v228, v89
	s_waitcnt lgkmcnt(0)
	v_mov_b32_e32 v229, v93
	v_mov_b32_e32 v200, v88
	v_mov_b32_e32 v201, v92
	v_pk_mul_f32 v[228:229], v[228:229], v[228:229]
	s_nop 0
	v_pk_fma_f32 v[200:201], v[200:201], v[200:201], v[228:229]
	v_mov_b32_e32 v228, v90
	v_mov_b32_e32 v229, v94
	v_pk_fma_f32 v[200:201], v[228:229], v[228:229], v[200:201]
	v_mov_b32_e32 v228, v91
	v_mov_b32_e32 v229, v95
	v_pk_fma_f32 v[200:201], v[228:229], v[228:229], v[200:201]
	ds_read_b128 v[228:231], v208
	ds_read_b128 v[232:235], v208 offset:16
	ds_read_b128 v[236:239], v208 offset:32
	ds_read_b128 v[240:243], v208 offset:48
	v_add_f32_e32 v200, v227, v200
	v_add_f32_e32 v200, v200, v201
	ds_swizzle_b32 v201, v200 offset:swizzle(SWAP,1)
	s_waitcnt lgkmcnt(0)
	v_add_f32_e32 v200, v200, v201
	ds_swizzle_b32 v201, v200 offset:swizzle(SWAP,2)
	s_waitcnt lgkmcnt(0)
	v_add_f32_e32 v200, v200, v201
	ds_swizzle_b32 v201, v200 offset:swizzle(SWAP,4)
	s_waitcnt lgkmcnt(0)
	v_add_f32_e32 v200, v200, v201
	v_fmamk_f32 v200, v200, 0x3b800000, v181
	v_rsq_f32_e32 v244, v200
	v_lshl_add_u64 v[200:201], s[76:77], 0, v[188:189]
	v_pk_mul_f32 v[66:67], v[66:67], v[244:245] op_sel_hi:[1,0]
	s_nop 0
	v_pk_mul_f32 v[66:67], v[230:231], v[66:67]
	v_pk_mul_f32 v[68:69], v[68:69], v[244:245] op_sel_hi:[1,0]
	v_pk_mul_f32 v[64:65], v[64:65], v[244:245] op_sel_hi:[1,0]
	v_pk_mul_f32 v[66:67], v[66:67], v[176:177]
	v_lshlrev_b32_e32 v176, 16, v178
	v_and_b32_e32 v177, 0xffff0000, v178
	v_pk_mul_f32 v[68:69], v[232:233], v[68:69]
	v_pk_mul_f32 v[70:71], v[70:71], v[244:245] op_sel_hi:[1,0]
	v_pk_mul_f32 v[64:65], v[228:229], v[64:65]
	v_pk_mul_f32 v[68:69], v[68:69], v[176:177]
	v_lshlrev_b32_e32 v176, 16, v179
	v_and_b32_e32 v177, 0xffff0000, v179
	v_pk_mul_f32 v[70:71], v[234:235], v[70:71]
	v_pk_mul_f32 v[64:65], v[64:65], v[246:247]
	v_pk_mul_f32 v[70:71], v[70:71], v[176:177]
	v_add_co_u32_e32 v176, vcc, s33, v200
	v_cvt_pk_bf16_f32 v64, v64, v65
	v_cvt_pk_bf16_f32 v65, v66, v67
	v_cvt_pk_bf16_f32 v66, v68, v69
	v_cvt_pk_bf16_f32 v67, v70, v71
	v_addc_co_u32_e32 v177, vcc, 0, v201, vcc
	global_store_dwordx4 v[176:177], v[64:67], off offset:2048
	v_pk_mul_f32 v[68:69], v[74:75], v[244:245] op_sel_hi:[1,0]
	v_pk_mul_f32 v[70:71], v[76:77], v[244:245] op_sel_hi:[1,0]
	v_pk_mul_f32 v[66:67], v[72:73], v[244:245] op_sel_hi:[1,0]
	s_waitcnt vmcnt(9)
; #define LAS __attribute__((address_space(3)))
; __device__ __forceinline__ unsigned cvt_pk_bf16(float lo, float hi) { const bf16x2_t r = __builtin_convertvector((f32x2_t){lo, hi}, bf16x2_t); return __builtin_bit_cast(unsigned, r); }
; __device__ __forceinline__ float bf_lo(unsigned w) { return __uint_as_float(w << 16); }
; __device__ __forceinline__ float bf_hi(unsigned w) { return __uint_as_float(w & 0xffff0000u); }
; __device__ __forceinline__ void gla_unit(LAS unsigned char* lds, const unsigned char* ws, const float* g_onorm, const int b, const int h, const int wv) {
;     ...
;         __syncthreads();
; #pragma unroll
;         for (int i = 0; i < 2; ++i) { const int c = tid + 512 * i, row = c >> 4, cc = (c & 15) * 16;
;             *(LAS u32x4*)(lds + L_Q + row * QS + cc) = qr[par][i]; *(LAS u32x4*)(lds + L_K + row * QS + cc) = kr[par][i]; }
; #pragma unroll
;         for (int i = 0; i < 4; ++i) { const int c = tid + 512 * i; *(LAS u32x4*)(lds + L_V + (c >> 5) * VS + (c & 31) * 16) = vr[par][i]; }
;         if (tid < 32) {
;             const float L2E_ = 1.4426950408889634f;
;             *(LAS f32x4*)&dec[tid * 4] = (f32x4){__builtin_amdgcn_exp2f(dr[0] * L2E_), __builtin_amdgcn_exp2f(dr[1] * L2E_), __builtin_amdgcn_exp2f(dr[2] * L2E_), __builtin_amdgcn_exp2f(dr[3] * L2E_)};
;         }
;     ...
;             bf16_t* mp = mix + (t0 + t) * DM + 1024 + h * 256 + 32 * g8;
; #pragma unroll
;             for (int x = 0; x < 4; ++x) {
;                 const u32x4 og = ogr[x];
;                 const f32x4 g0 = *(const LAS f32x4*)&gon[32 * g8 + 8 * x], g1 = *(const LAS f32x4*)&gon[32 * g8 + 8 * x + 4];
;                 const float gg2[8] = {g0[0], g0[1], g0[2], g0[3], g1[0], g1[1], g1[2], g1[3]};
;                 float res[8];
; #pragma unroll
;                 for (int y = 0; y < 4; ++y) { const float a0 = bf_lo(og[y]), a1 = bf_hi(og[y]);
;                     res[2 * y] = ov[8 * x + 2 * y] * rstd * gg2[2 * y] * a0;
;                     res[2 * y + 1] = ov[8 * x + 2 * y + 1] * rstd * gg2[2 * y + 1] * a1; }
;                 u32x4 wv4; wv4[0] = cvt_pk_bf16(res[0], res[1]); wv4[1] = cvt_pk_bf16(res[2], res[3]); wv4[2] = cvt_pk_bf16(res[4], res[5]); wv4[3] = cvt_pk_bf16(res[6], res[7]);
;                 *(u32x4*)(mp + 8 * x) = wv4;
;             }
	v_lshlrev_b32_e32 v64, 16, v172
	v_and_b32_e32 v65, 0xffff0000, v172
	v_pk_mul_f32 v[66:67], v[236:237], v[66:67]
	v_pk_mul_f32 v[68:69], v[238:239], v[68:69]
	v_pk_mul_f32 v[64:65], v[66:67], v[64:65]
	v_lshlrev_b32_e32 v66, 16, v173
	v_and_b32_e32 v67, 0xffff0000, v173
	v_pk_mul_f32 v[66:67], v[68:69], v[66:67]
	v_lshlrev_b32_e32 v68, 16, v174
	v_and_b32_e32 v69, 0xffff0000, v174
	v_pk_mul_f32 v[70:71], v[240:241], v[70:71]
	v_pk_mul_f32 v[72:73], v[78:79], v[244:245] op_sel_hi:[1,0]
	v_pk_mul_f32 v[68:69], v[70:71], v[68:69]
	v_lshlrev_b32_e32 v70, 16, v175
	v_and_b32_e32 v71, 0xffff0000, v175
	v_pk_mul_f32 v[72:73], v[242:243], v[72:73]
	v_cvt_pk_bf16_f32 v64, v64, v65
	v_pk_mul_f32 v[70:71], v[72:73], v[70:71]
	v_cvt_pk_bf16_f32 v65, v66, v67
	v_cvt_pk_bf16_f32 v66, v68, v69
	v_cvt_pk_bf16_f32 v67, v70, v71
	global_store_dwordx4 v[176:177], v[64:67], off offset:2064
	ds_read_b128 v[64:67], v208 offset:64
	ds_read_b128 v[68:71], v208 offset:80
	v_pk_mul_f32 v[74:75], v[80:81], v[244:245] op_sel_hi:[1,0]
	v_lshlrev_b32_e32 v72, 16, v168
	v_and_b32_e32 v73, 0xffff0000, v168
	s_waitcnt lgkmcnt(1)
	v_pk_mul_f32 v[64:65], v[64:65], v[74:75]
	v_pk_mul_f32 v[74:75], v[82:83], v[244:245] op_sel_hi:[1,0]
	v_pk_mul_f32 v[64:65], v[64:65], v[72:73]
	v_lshlrev_b32_e32 v72, 16, v169
	v_and_b32_e32 v73, 0xffff0000, v169
	v_pk_mul_f32 v[66:67], v[66:67], v[74:75]
	v_pk_mul_f32 v[74:75], v[84:85], v[244:245] op_sel_hi:[1,0]
	v_pk_mul_f32 v[66:67], v[66:67], v[72:73]
	v_lshlrev_b32_e32 v72, 16, v170
	v_and_b32_e32 v73, 0xffff0000, v170
	s_waitcnt lgkmcnt(0)
	v_pk_mul_f32 v[68:69], v[68:69], v[74:75]
	v_pk_mul_f32 v[74:75], v[86:87], v[244:245] op_sel_hi:[1,0]
	v_pk_mul_f32 v[68:69], v[68:69], v[72:73]
	v_lshlrev_b32_e32 v72, 16, v171
	v_and_b32_e32 v73, 0xffff0000, v171
	v_pk_mul_f32 v[70:71], v[70:71], v[74:75]
	v_cvt_pk_bf16_f32 v64, v64, v65
	v_pk_mul_f32 v[70:71], v[70:71], v[72:73]
	v_cvt_pk_bf16_f32 v65, v66, v67
	v_cvt_pk_bf16_f32 v66, v68, v69
	v_cvt_pk_bf16_f32 v67, v70, v71
	global_store_dwordx4 v[176:177], v[64:67], off offset:2080
	ds_read_b128 v[64:67], v208 offset:96
	ds_read_b128 v[68:71], v208 offset:112
	v_pk_mul_f32 v[74:75], v[88:89], v[244:245] op_sel_hi:[1,0]
	v_lshlrev_b32_e32 v72, 16, v164
	v_and_b32_e32 v73, 0xffff0000, v164
	s_waitcnt lgkmcnt(1)
	v_pk_mul_f32 v[64:65], v[74:75], v[64:65]
	v_pk_mul_f32 v[74:75], v[90:91], v[244:245] op_sel_hi:[1,0]
	v_pk_mul_f32 v[64:65], v[64:65], v[72:73]
	v_lshlrev_b32_e32 v72, 16, v165
	v_and_b32_e32 v73, 0xffff0000, v165
	v_pk_mul_f32 v[66:67], v[74:75], v[66:67]
	v_pk_mul_f32 v[74:75], v[92:93], v[244:245] op_sel_hi:[1,0]
	v_pk_mul_f32 v[66:67], v[66:67], v[72:73]
	v_lshlrev_b32_e32 v72, 16, v166
	v_and_b32_e32 v73, 0xffff0000, v166
	s_waitcnt lgkmcnt(0)
	v_pk_mul_f32 v[68:69], v[74:75], v[68:69]
	v_pk_mul_f32 v[74:75], v[94:95], v[244:245] op_sel_hi:[1,0]
	v_pk_mul_f32 v[68:69], v[68:69], v[72:73]
	v_lshlrev_b32_e32 v72, 16, v167
	v_and_b32_e32 v73, 0xffff0000, v167
	v_pk_mul_f32 v[70:71], v[74:75], v[70:71]
	v_cvt_pk_bf16_f32 v64, v64, v65
	v_pk_mul_f32 v[70:71], v[70:71], v[72:73]
	v_cvt_pk_bf16_f32 v65, v66, v67
	v_cvt_pk_bf16_f32 v66, v68, v69
	v_cvt_pk_bf16_f32 v67, v70, v71
	global_store_dwordx4 v[176:177], v[64:67], off offset:2096
	s_barrier
	s_waitcnt vmcnt(20)
	ds_write_b128 v209, v[132:135]
	ds_write_b128 v209, v[136:139] offset:17408
	ds_write_b128 v210, v[140:143]
	ds_write_b128 v210, v[144:147] offset:17408
	ds_write_b128 v211, v[148:151]
	ds_write_b128 v212, v[152:155]
	ds_write_b128 v213, v[156:159]
	ds_write_b128 v214, v[160:163]
	s_and_saveexec_b64 s[42:43], s[0:1]
	s_cbranch_execz .LBB0_648
	s_waitcnt vmcnt(12)
	v_mul_f32_e32 v64, 0x3fb8aa3b, v124
	v_mul_f32_e32 v65, 0x3fb8aa3b, v125
	v_mul_f32_e32 v66, 0x3fb8aa3b, v126
	v_mul_f32_e32 v67, 0x3fb8aa3b, v127
	v_exp_f32_e32 v64, v64
	v_exp_f32_e32 v65, v65
	v_exp_f32_e32 v66, v66
	v_exp_f32_e32 v67, v67
	ds_write_b128 v226, v[64:67]

; #define LAS __attribute__((address_space(3)))
; __device__ __forceinline__ void gla_unit(LAS unsigned char* lds, const unsigned char* ws, const float* g_onorm, const int b, const int h, const int wv) {
;     ...
;         f32x16 O[2];
; #pragma unroll
;         for (int tt = 0; tt < 2; ++tt)
; #pragma unroll
;             for (int r = 0; r < 16; ++r) O[tt][r] = 0.f;
; #pragma unroll
;         for (int et = 0; et < 4; ++et)
; #pragma unroll
;             for (int s2 = 0; s2 < 2; ++s2) {
;                 const bf16x8 sb = pack8(S[et], s2);
; #pragma unroll
;                 for (int tt = 0; tt < 2; ++tt) {
;                     const bf16x8 aq = ld2x64(qb8 + 32 * tt * QS + (32 * et + 16 * s2) * 2);
;                     O[tt] = __builtin_amdgcn_mfma_f32_32x32x16_bf16(aq, sb, O[tt], 0, 0, 0);
;                 }
;             }
;         __syncthreads();
; #pragma unroll
;         for (int pr = 0; pr < 3; ++pr) {
;             const int st = (pr == 2) ? 1 : 0, tt = (pr == 0) ? 0 : 1;
; #pragma unroll
;             for (int s2 = 0; s2 < 2; ++s2) {
;                 const bf16x8 ax = *(const LAS bf16x8*)(frb + (pr * 2 + s2) * 1024);
;                 const LAS unsigned char* vp = vP + (32 * st + 16 * s2) * VS;
;                 const bf16x8 bv = tr8(vp, vp + 8 * VS);
;                 O[tt] = __builtin_amdgcn_mfma_f32_32x32x16_bf16(ax, bv, O[tt], 0, 0, 0);
;             }
;         }
;         __builtin_amdgcn_sched_barrier(0);
; #pragma unroll
;         for (int tt = 0; tt < 2; ++tt)
; #pragma unroll
;             for (int r = 0; r < 16; ++r) ob[(32 * tt + (r & 3) + 8 * (r >> 2)) * OS] = O[tt][r];
;         __builtin_amdgcn_sched_barrier(0);
; #pragma unroll
;         for (int et = 0; et < 4; ++et)
; #pragma unroll
;             for (int rg = 0; rg < 4; ++rg) { const f32x4 dl = *(const LAS f32x4*)&decb[32 * et + 8 * rg];
.LBB0_1692:
	ds_read2_b64 v[64:67], v222 offset1:2
	v_cvt_pk_bf16_f32 v68, v48, v49
	v_cvt_pk_bf16_f32 v69, v50, v51
	v_cvt_pk_bf16_f32 v70, v52, v53
	v_cvt_pk_bf16_f32 v71, v54, v55
	ds_read2_b64 v[192:195], v222 offset0:4 offset1:6
	v_cvt_pk_bf16_f32 v198, v56, v57
	v_cvt_pk_bf16_f32 v199, v58, v59
	v_cvt_pk_bf16_f32 v200, v60, v61
	s_waitcnt lgkmcnt(1)
	v_mfma_f32_32x32x16_bf16 v[80:95], v[64:67], v[68:71], 0
	ds_read2_b64 v[64:67], v223 offset0:64 offset1:66
	v_cvt_pk_bf16_f32 v201, v62, v63
	s_waitcnt lgkmcnt(1)
	s_nop 0
	v_mfma_f32_32x32x16_bf16 v[80:95], v[192:195], v[198:201], v[80:95]
	ds_read2_b64 v[192:195], v223 offset0:68 offset1:70
	s_waitcnt lgkmcnt(1)
	v_mfma_f32_32x32x16_bf16 v[64:79], v[64:67], v[68:71], 0
	s_waitcnt lgkmcnt(0)
	v_mfma_f32_32x32x16_bf16 v[64:79], v[192:195], v[198:201], v[64:79]
	ds_read2_b64 v[192:195], v222 offset0:8 offset1:10
	ds_read2_b64 v[224:227], v223 offset0:72 offset1:74
	ds_read2_b64 v[232:235], v222 offset0:12 offset1:14
	v_cvt_pk_bf16_f32 v198, v16, v17
	v_cvt_pk_bf16_f32 v199, v18, v19
	v_cvt_pk_bf16_f32 v200, v20, v21
	v_cvt_pk_bf16_f32 v201, v22, v23
	s_waitcnt lgkmcnt(2)
	s_nop 0
	v_mfma_f32_32x32x16_bf16 v[80:95], v[192:195], v[198:201], v[80:95]
	ds_read2_b64 v[236:239], v223 offset0:76 offset1:78
	s_waitcnt lgkmcnt(2)
	v_mfma_f32_32x32x16_bf16 v[64:79], v[224:227], v[198:201], v[64:79]
	ds_read2_b64 v[192:195], v222 offset0:16 offset1:18
	v_cvt_pk_bf16_f32 v198, v24, v25
	v_cvt_pk_bf16_f32 v199, v26, v27
	v_cvt_pk_bf16_f32 v200, v28, v29
	v_cvt_pk_bf16_f32 v201, v30, v31
	s_waitcnt lgkmcnt(2)
	s_nop 0
	v_mfma_f32_32x32x16_bf16 v[80:95], v[232:235], v[198:201], v[80:95]
	ds_read2_b64 v[224:227], v223 offset0:80 offset1:82
	s_waitcnt lgkmcnt(2)
	v_mfma_f32_32x32x16_bf16 v[64:79], v[236:239], v[198:201], v[64:79]
	ds_read2_b64 v[232:235], v222 offset0:20 offset1:22
	v_cvt_pk_bf16_f32 v198, v32, v33
	v_cvt_pk_bf16_f32 v199, v34, v35
	v_cvt_pk_bf16_f32 v200, v36, v37
	v_cvt_pk_bf16_f32 v201, v38, v39
	s_waitcnt lgkmcnt(2)
	s_nop 0
	v_mfma_f32_32x32x16_bf16 v[80:95], v[192:195], v[198:201], v[80:95]
	ds_read2_b64 v[236:239], v223 offset0:84 offset1:86
	s_waitcnt lgkmcnt(2)
	v_mfma_f32_32x32x16_bf16 v[64:79], v[224:227], v[198:201], v[64:79]
	ds_read2_b64 v[192:195], v222 offset0:24 offset1:26
	v_cvt_pk_bf16_f32 v198, v40, v41
	v_cvt_pk_bf16_f32 v199, v42, v43
	v_cvt_pk_bf16_f32 v200, v44, v45
	v_cvt_pk_bf16_f32 v201, v46, v47
	s_waitcnt lgkmcnt(2)
	s_nop 0
	v_mfma_f32_32x32x16_bf16 v[80:95], v[232:235], v[198:201], v[80:95]
	ds_read2_b64 v[224:227], v223 offset0:88 offset1:90
	s_waitcnt lgkmcnt(2)
	v_mfma_f32_32x32x16_bf16 v[64:79], v[236:239], v[198:201], v[64:79]
	ds_read2_b64 v[232:235], v222 offset0:28 offset1:30
	v_cvt_pk_bf16_f32 v198, v0, v1
	v_cvt_pk_bf16_f32 v199, v2, v3
	v_cvt_pk_bf16_f32 v200, v4, v5
	v_cvt_pk_bf16_f32 v201, v6, v7
	s_waitcnt lgkmcnt(2)
	s_nop 0
	v_mfma_f32_32x32x16_bf16 v[80:95], v[192:195], v[198:201], v[80:95]
	ds_read2_b64 v[236:239], v223 offset0:92 offset1:94
	s_waitcnt lgkmcnt(2)
	v_mfma_f32_32x32x16_bf16 v[64:79], v[224:227], v[198:201], v[64:79]
	v_cvt_pk_bf16_f32 v198, v8, v9
	v_cvt_pk_bf16_f32 v199, v10, v11
	v_cvt_pk_bf16_f32 v200, v12, v13
	v_cvt_pk_bf16_f32 v201, v14, v15
	s_waitcnt lgkmcnt(1)
	s_nop 0
	v_mfma_f32_32x32x16_bf16 v[80:95], v[232:235], v[198:201], v[80:95]
	s_waitcnt lgkmcnt(0)
	s_barrier
	v_mfma_f32_32x32x16_bf16 v[64:79], v[236:239], v[198:201], v[64:79]
	ds_read_b128 v[192:195], v206
	ds_read_b64_tr_b16 v[198:199], v218
	ds_read_b64_tr_b16 v[200:201], v218 offset:4608
	ds_read_b128 v[222:225], v206 offset:1024
	ds_read_b64_tr_b16 v[226:227], v218 offset:9216
	ds_read_b64_tr_b16 v[228:229], v218 offset:13824
	s_waitcnt lgkmcnt(3)
	v_mfma_f32_32x32x16_bf16 v[80:95], v[192:195], v[198:201], v[80:95]
	s_waitcnt lgkmcnt(0)
	v_mfma_f32_32x32x16_bf16 v[80:95], v[222:225], v[226:229], v[80:95]
	ds_read_b128 v[192:195], v206 offset:2048
	ds_read_b128 v[222:225], v206 offset:3072
	s_waitcnt lgkmcnt(1)
	v_mfma_f32_32x32x16_bf16 v[64:79], v[192:195], v[198:201], v[64:79]
	s_waitcnt lgkmcnt(0)
	v_mfma_f32_32x32x16_bf16 v[64:79], v[222:225], v[226:229], v[64:79]
	ds_read_b128 v[192:195], v206 offset:4096
	ds_read_b64_tr_b16 v[198:199], v218 offset:18432
	ds_read_b64_tr_b16 v[200:201], v218 offset:23040
	ds_read_b128 v[222:225], v206 offset:5120
	ds_read_b64_tr_b16 v[226:227], v218 offset:27648
	ds_read_b64_tr_b16 v[228:229], v218 offset:32256
	s_waitcnt lgkmcnt(3)
	v_mfma_f32_32x32x16_bf16 v[64:79], v[192:195], v[198:201], v[64:79]
	s_waitcnt lgkmcnt(0)
	v_mfma_f32_32x32x16_bf16 v[64:79], v[222:225], v[226:229], v[64:79]
	ds_write_b32 v207, v80
	ds_write_b32 v207, v81 offset:1040
	ds_write_b32 v207, v82 offset:2080
	ds_write_b32 v207, v83 offset:3120
	ds_write_b32 v207, v84 offset:8320
	ds_write_b32 v207, v85 offset:9360
	ds_write_b32 v207, v86 offset:10400
	ds_write_b32 v207, v87 offset:11440
	ds_write_b32 v207, v88 offset:16640
	ds_write_b32 v207, v89 offset:17680
	ds_write_b32 v207, v90 offset:18720
	ds_write_b32 v207, v91 offset:19760
	ds_write_b32 v207, v92 offset:24960
	ds_write_b32 v207, v93 offset:26000
	ds_write_b32 v207, v94 offset:27040
	ds_write_b32 v207, v95 offset:28080
	ds_write_b32 v207, v64 offset:33280
	ds_write_b32 v207, v65 offset:34320
	ds_write_b32 v207, v66 offset:35360
	ds_write_b32 v207, v67 offset:36400
	ds_write_b32 v207, v68 offset:41600
	ds_write_b32 v207, v69 offset:42640
	ds_write_b32 v207, v70 offset:43680
	ds_write_b32 v207, v71 offset:44720
	ds_write_b32 v207, v72 offset:49920
	ds_write_b32 v207, v73 offset:50960
	ds_write_b32 v207, v74 offset:52000
	ds_write_b32 v207, v75 offset:53040
	ds_write_b32 v207, v76 offset:58240
	ds_write_b32 v207, v77 offset:59280
	ds_write_b32 v207, v78 offset:60320
	ds_write_b32 v207, v79 offset:61360
	ds_read_b128 v[64:67], v205 offset:96
	ds_read_b128 v[68:71], v205 offset:64
	ds_read_b128 v[72:75], v205 offset:32
	ds_read_b128 v[76:79], v205
	s_waitcnt vmcnt(11)
; #define LAS __attribute__((address_space(3)))
; __device__ __forceinline__ void gla_unit(LAS unsigned char* lds, const unsigned char* ws, const float* g_onorm, const int b, const int h, const int wv) {
;     ...
; #pragma unroll
;         for (int et = 0; et < 4; ++et)
; #pragma unroll
;             for (int rg = 0; rg < 4; ++rg) { const f32x4 dl = *(const LAS f32x4*)&decb[32 * et + 8 * rg];
; #pragma unroll
;                 for (int x = 0; x < 4; ++x) S[et][4 * rg + x] *= dl[x]; }
; #pragma unroll
;         for (int ks = 0; ks < 4; ++ks) {
;             const LAS unsigned char* vp = vN + 16 * ks * VS;
;             const bf16x8 bv = tr8(vp, vp + 4 * VS);
; #pragma unroll
;             for (int et = 0; et < 4; ++et) {
;                 const LAS unsigned char* kp = keN + 32 * et * 2 + 16 * ks * ES;
;                 const bf16x8 ak = tr8(kp, kp + 4 * ES);
;                 S[et] = __builtin_amdgcn_mfma_f32_32x32x16_bf16(ak, bv, S[et], 0, 0, 0);
;             }
;         }
	v_lshlrev_b32_e32 v232, 16, v176
	s_waitcnt lgkmcnt(3)
	v_mul_f32_e32 v62, v62, v66
	v_mul_f32_e32 v63, v63, v67
	s_waitcnt lgkmcnt(2)
	v_mul_f32_e32 v58, v58, v70
	v_mul_f32_e32 v59, v59, v71
	v_mul_f32_e32 v60, v60, v64
	v_mul_f32_e32 v61, v61, v65
	s_waitcnt lgkmcnt(0)
	v_mul_f32_e32 v50, v50, v78
	v_mul_f32_e32 v51, v51, v79
	v_mul_f32_e32 v56, v56, v68
	v_mul_f32_e32 v57, v57, v69
	ds_read_b128 v[64:67], v205 offset:192
	ds_read_b128 v[68:71], v205 offset:224
	ds_read_b128 v[78:81], v205 offset:128
	ds_read_b128 v[82:85], v205 offset:160
	v_mul_f32_e32 v54, v54, v74
	v_mul_f32_e32 v55, v55, v75
	v_mul_f32_e32 v52, v52, v72
	v_mul_f32_e32 v53, v53, v73
	v_mul_f32_e32 v48, v48, v76
	v_mul_f32_e32 v49, v49, v77
	s_waitcnt lgkmcnt(2)
	v_mul_f32_e32 v30, v30, v70
	v_mul_f32_e32 v31, v31, v71
	v_mul_f32_e32 v26, v26, v66
	v_mul_f32_e32 v27, v27, v67
	s_waitcnt lgkmcnt(0)
	v_mul_f32_e32 v22, v22, v84
	v_mul_f32_e32 v23, v23, v85
	v_mul_f32_e32 v18, v18, v80
	v_mul_f32_e32 v19, v19, v81
	v_mul_f32_e32 v28, v28, v68
	v_mul_f32_e32 v29, v29, v69
	v_mul_f32_e32 v24, v24, v64
	v_mul_f32_e32 v25, v25, v65
	v_mul_f32_e32 v20, v20, v82
	v_mul_f32_e32 v21, v21, v83
	ds_read_b128 v[64:67], v205 offset:256
	ds_read_b128 v[68:71], v205 offset:288
	ds_read_b128 v[72:75], v205 offset:320
	ds_read_b128 v[80:83], v205 offset:352
	ds_read_b64_tr_b16 v[84:85], v219
	ds_read_b64_tr_b16 v[86:87], v219 offset:2304
	ds_read_b64_tr_b16 v[90:91], v220 offset:1280
	ds_read_b64_tr_b16 v[88:89], v220
	ds_read_b64_tr_b16 v[92:93], v220 offset:64
	ds_read_b64_tr_b16 v[192:193], v220 offset:128
	ds_read_b64_tr_b16 v[198:199], v220 offset:192
	ds_read_b64_tr_b16 v[94:95], v220 offset:1344
	ds_read_b64_tr_b16 v[194:195], v220 offset:1408
	ds_read_b64_tr_b16 v[200:201], v220 offset:1472
	ds_read_b64_tr_b16 v[222:223], v219 offset:9216
	ds_read_b64_tr_b16 v[224:225], v219 offset:11520
	s_waitcnt lgkmcnt(8)
	v_mfma_f32_32x32x16_bf16 v[48:63], v[88:91], v[84:87], v[48:63]
	v_mul_f32_e64 v16, v16, v78
	v_mul_f32_e64 v17, v17, v79
	v_mul_f32_e64 v42, v42, v74
	v_mul_f32_e64 v43, v43, v75
	v_mul_f32_e64 v38, v38, v70
	v_mul_f32_e64 v39, v39, v71
	v_mul_f32_e32 v34, v34, v66
	v_mul_f32_e32 v35, v35, v67
	v_mul_f32_e32 v44, v44, v80
	v_mul_f32_e32 v45, v45, v81
	v_mul_f32_e32 v40, v40, v72
	v_mul_f32_e32 v41, v41, v73
	ds_read_b128 v[70:73], v205 offset:448
	ds_read_b128 v[74:77], v205 offset:480
	v_mul_f32_e32 v36, v36, v68
	v_mul_f32_e32 v37, v37, v69
	ds_read_b128 v[66:69], v205 offset:384
	ds_read_b128 v[78:81], v205 offset:416
	v_mul_f32_e32 v46, v46, v82
	v_mul_f32_e32 v47, v47, v83
	v_mul_f32_e32 v32, v32, v64
	v_mul_f32_e32 v33, v33, v65
	s_waitcnt lgkmcnt(2)
	v_mul_f32_e32 v14, v14, v76
	v_mul_f32_e32 v15, v15, v77
	v_mul_f32_e32 v10, v10, v72
	v_mul_f32_e32 v11, v11, v73
	s_waitcnt lgkmcnt(0)
	v_mul_f32_e32 v6, v6, v80
	v_mul_f32_e32 v7, v7, v81
	v_mul_f32_e32 v2, v2, v68
	v_mul_f32_e32 v3, v3, v69
	v_mul_f32_e32 v12, v12, v74
	v_mul_f32_e32 v13, v13, v75
	v_mul_f32_e32 v8, v8, v70
	v_mul_f32_e32 v9, v9, v71
	v_mul_f32_e32 v4, v4, v78
	v_mul_f32_e32 v5, v5, v79
	v_mul_f32_e32 v0, v0, v66
	v_mul_f32_e32 v1, v1, v67
	v_mfma_f32_32x32x16_bf16 v[16:31], v[92:95], v[84:87], v[16:31]
	ds_read_b64_tr_b16 v[66:67], v220 offset:6400
	ds_read_b64_tr_b16 v[64:65], v220 offset:5120
	ds_read_b64_tr_b16 v[68:69], v220 offset:5184
	ds_read_b64_tr_b16 v[72:73], v220 offset:5248
	ds_read_b64_tr_b16 v[76:77], v220 offset:5312
	ds_read_b64_tr_b16 v[70:71], v220 offset:6464
	ds_read_b64_tr_b16 v[74:75], v220 offset:6528
	ds_read_b64_tr_b16 v[78:79], v220 offset:6592
	v_and_b32_e32 v233, 0xffff0000, v176
	s_add_i32 s66, s66, 2
	v_lshl_add_u64 v[182:183], v[182:183], 0, s[60:61]
	v_lshl_add_u64 v[184:185], v[184:185], 0, s[62:63]
	v_lshl_add_u64 v[186:187], v[186:187], 0, s[64:65]
	v_lshl_add_u64 v[188:189], v[188:189], 0, s[68:69]
	v_mfma_f32_32x32x16_bf16 v[32:47], v[192:195], v[84:87], v[32:47]
	s_cmp_lt_u32 s73, 30
	v_lshl_add_u64 v[190:191], v[190:191], 0, s[62:63]
	v_mfma_f32_32x32x16_bf16 v[0:15], v[198:201], v[84:87], v[0:15]
	s_waitcnt lgkmcnt(6)
	v_mfma_f32_32x32x16_bf16 v[48:63], v[64:67], v[222:225], v[48:63]
	s_waitcnt lgkmcnt(2)
	v_mfma_f32_32x32x16_bf16 v[16:31], v[68:71], v[222:225], v[16:31]
	s_waitcnt lgkmcnt(1)
	v_mfma_f32_32x32x16_bf16 v[32:47], v[72:75], v[222:225], v[32:47]
	s_waitcnt lgkmcnt(0)
	v_mfma_f32_32x32x16_bf16 v[0:15], v[76:79], v[222:225], v[0:15]
	ds_read_b64_tr_b16 v[64:65], v219 offset:18432
	ds_read_b64_tr_b16 v[66:67], v219 offset:20736
	ds_read_b64_tr_b16 v[70:71], v220 offset:11520
	ds_read_b64_tr_b16 v[68:69], v220 offset:10240
	ds_read_b64_tr_b16 v[72:73], v220 offset:10304
	ds_read_b64_tr_b16 v[76:77], v220 offset:10368
	ds_read_b64_tr_b16 v[80:81], v220 offset:10432
	ds_read_b64_tr_b16 v[74:75], v220 offset:11584
	ds_read_b64_tr_b16 v[78:79], v220 offset:11648
	ds_read_b64_tr_b16 v[82:83], v220 offset:11712
	ds_read_b64_tr_b16 v[84:85], v219 offset:27648
	ds_read_b64_tr_b16 v[86:87], v219 offset:29952
	s_waitcnt lgkmcnt(8)
	v_mfma_f32_32x32x16_bf16 v[48:63], v[68:71], v[64:67], v[48:63]
	ds_read_b64_tr_b16 v[68:69], v220 offset:16640
	s_waitcnt lgkmcnt(5)
	v_mfma_f32_32x32x16_bf16 v[16:31], v[72:75], v[64:67], v[16:31]
	s_waitcnt lgkmcnt(4)
	v_mfma_f32_32x32x16_bf16 v[32:47], v[76:79], v[64:67], v[32:47]
	s_waitcnt lgkmcnt(3)
	v_mfma_f32_32x32x16_bf16 v[0:15], v[80:83], v[64:67], v[0:15]
	ds_read_b64_tr_b16 v[66:67], v220 offset:15360
	ds_read_b64_tr_b16 v[70:71], v220 offset:15424
	ds_read_b64_tr_b16 v[74:75], v220 offset:15488
	ds_read_b64_tr_b16 v[78:79], v220 offset:15552
	ds_read_b64_tr_b16 v[72:73], v220 offset:16704
	ds_read_b64_tr_b16 v[76:77], v220 offset:16768
	ds_read_b64_tr_b16 v[80:81], v220 offset:16832
	s_waitcnt lgkmcnt(0)
	s_barrier
; #define LAS __attribute__((address_space(3)))
; __device__ __forceinline__ unsigned cvt_pk_bf16(float lo, float hi) { const bf16x2_t r = __builtin_convertvector((f32x2_t){lo, hi}, bf16x2_t); return __builtin_bit_cast(unsigned, r); }
; __device__ __forceinline__ float bf_lo(unsigned w) { return __uint_as_float(w << 16); }
; __device__ __forceinline__ float bf_hi(unsigned w) { return __uint_as_float(w & 0xffff0000u); }
; __device__ __forceinline__ void gla_unit(LAS unsigned char* lds, const unsigned char* ws, const float* g_onorm, const int b, const int h, const int wv) {
;     ...
;         {
;             const int t = tid >> 3, g8 = tid & 7;
;             float ov[32]; float ss = 0.f;
; #pragma unroll
;             for (int x = 0; x < 8; ++x) { const f32x4 v = *(const LAS f32x4*)&obuf[t * OS + 32 * g8 + 4 * x]; ov[4 * x] = v[0]; ov[4 * x + 1] = v[1]; ov[4 * x + 2] = v[2]; ov[4 * x + 3] = v[3];
;                 ss += v[0] * v[0] + v[1] * v[1] + v[2] * v[2] + v[3] * v[3]; }
;             ss += __builtin_bit_cast(float, __builtin_amdgcn_ds_swizzle(__builtin_bit_cast(int, ss), (1 << 10) | 0x1F)); ss += __builtin_bit_cast(float, __builtin_amdgcn_ds_swizzle(__builtin_bit_cast(int, ss), (2 << 10) | 0x1F));
;             ss += __builtin_bit_cast(float, __builtin_amdgcn_ds_swizzle(__builtin_bit_cast(int, ss), (4 << 10) | 0x1F));
;             const float rstd = __builtin_amdgcn_rsqf(ss * (1.0f / 256.0f) + EPSV);
;             bf16_t* mp = mix + (t0 + t) * DM + 1024 + h * 256 + 32 * g8;
; #pragma unroll
;             for (int x = 0; x < 4; ++x) {
;                 const u32x4 og = ogr[x];
;                 const f32x4 g0 = *(const LAS f32x4*)&gon[32 * g8 + 8 * x], g1 = *(const LAS f32x4*)&gon[32 * g8 + 8 * x + 4];
;                 const float gg2[8] = {g0[0], g0[1], g0[2], g0[3], g1[0], g1[1], g1[2], g1[3]};
;                 float res[8];
; #pragma unroll
;                 for (int y = 0; y < 4; ++y) { const float a0 = bf_lo(og[y]), a1 = bf_hi(og[y]);
;                     res[2 * y] = ov[8 * x + 2 * y] * rstd * gg2[2 * y] * a0;
;                     res[2 * y + 1] = ov[8 * x + 2 * y + 1] * rstd * gg2[2 * y + 1] * a1; }
;                 u32x4 wv4; wv4[0] = cvt_pk_bf16(res[0], res[1]); wv4[1] = cvt_pk_bf16(res[2], res[3]); wv4[2] = cvt_pk_bf16(res[4], res[5]); wv4[3] = cvt_pk_bf16(res[6], res[7]);
;                 *(u32x4*)(mp + 8 * x) = wv4;
;             }
	v_mfma_f32_32x32x16_bf16 v[48:63], v[66:69], v[84:87], v[48:63]
	ds_read_b128 v[64:67], v221
	ds_read_b128 v[88:91], v221 offset:16
	ds_read_b128 v[92:95], v221 offset:32
	ds_read_b128 v[192:195], v221 offset:48
	s_waitcnt lgkmcnt(3)
	v_mul_f32_e32 v68, v65, v65
	s_waitcnt lgkmcnt(2)
	v_mul_f32_e32 v69, v89, v89
	v_fmac_f32_e32 v68, v64, v64
	v_fmac_f32_e32 v69, v88, v88
	v_fmac_f32_e32 v68, v66, v66
	v_fmac_f32_e32 v69, v90, v90
	v_mfma_f32_32x32x16_bf16 v[16:31], v[70:73], v[84:87], v[16:31]
	v_fmac_f32_e32 v68, v67, v67
	v_fmac_f32_e32 v69, v91, v91
	s_waitcnt lgkmcnt(1)
	v_mov_b32_e32 v70, v93
	s_waitcnt lgkmcnt(0)
	v_mov_b32_e32 v71, v193
	v_add_f32_e32 v222, v68, v69
	v_mov_b32_e32 v68, v92
	v_mov_b32_e32 v69, v192
	v_pk_mul_f32 v[70:71], v[70:71], v[70:71]
	v_mov_b32_e32 v82, v95
	v_pk_fma_f32 v[68:69], v[68:69], v[68:69], v[70:71]
	v_mov_b32_e32 v70, v94
	v_mov_b32_e32 v71, v194
	v_pk_fma_f32 v[72:73], v[70:71], v[70:71], v[68:69]
	ds_read_b128 v[68:71], v221 offset:64
	ds_read_b128 v[198:201], v221 offset:80
	v_mov_b32_e32 v83, v195
	v_pk_fma_f32 v[72:73], v[82:83], v[82:83], v[72:73]
	v_mfma_f32_32x32x16_bf16 v[32:47], v[74:77], v[84:87], v[32:47]
	v_add_f32_e32 v72, v222, v72
	s_waitcnt lgkmcnt(1)
	v_mov_b32_e32 v82, v69
	s_waitcnt lgkmcnt(0)
	v_mov_b32_e32 v83, v199
	ds_read_b128 v[222:225], v221 offset:96
	ds_read_b128 v[226:229], v221 offset:112
	v_add_f32_e32 v230, v72, v73
	v_mov_b32_e32 v72, v68
	v_mov_b32_e32 v73, v198
	v_pk_mul_f32 v[82:83], v[82:83], v[82:83]
	v_mfma_f32_32x32x16_bf16 v[0:15], v[78:81], v[84:87], v[0:15]
	v_fma_f32 v72, v72, v72, v82
	v_fma_f32 v73, v73, v73, v83
	v_mov_b32_e32 v82, v70
	v_mov_b32_e32 v83, v200
	v_fma_f32 v72, v82, v82, v72
	v_fma_f32 v73, v83, v83, v73
	v_mov_b32_e32 v82, v71
	v_mov_b32_e32 v83, v201
	v_pk_fma_f32 v[72:73], v[82:83], v[82:83], v[72:73]
	s_waitcnt lgkmcnt(1)
	v_mov_b32_e32 v82, v223
	v_add_f32_e32 v72, v230, v72
	s_waitcnt lgkmcnt(0)
	v_mov_b32_e32 v83, v227
	v_add_f32_e32 v230, v72, v73
	v_mov_b32_e32 v72, v222
	v_mov_b32_e32 v73, v226
	v_pk_mul_f32 v[82:83], v[82:83], v[82:83]
	s_nop 0
	v_pk_fma_f32 v[72:73], v[72:73], v[72:73], v[82:83]
	v_mov_b32_e32 v82, v224
	v_mov_b32_e32 v83, v228
	v_pk_fma_f32 v[72:73], v[82:83], v[82:83], v[72:73]
	v_mov_b32_e32 v82, v225
	v_mov_b32_e32 v83, v229
	v_pk_fma_f32 v[72:73], v[82:83], v[82:83], v[72:73]
	s_nop 0
	v_add_f32_e32 v72, v230, v72
	v_add_f32_e32 v72, v72, v73
	ds_swizzle_b32 v73, v72 offset:swizzle(SWAP,1)
	s_waitcnt lgkmcnt(0)
	v_add_f32_e32 v72, v72, v73
	ds_swizzle_b32 v73, v72 offset:swizzle(SWAP,2)
	s_waitcnt lgkmcnt(0)
	v_add_f32_e32 v72, v72, v73
	ds_swizzle_b32 v73, v72 offset:swizzle(SWAP,4)
	s_waitcnt lgkmcnt(0)
	v_add_f32_e32 v72, v72, v73
	v_fmamk_f32 v72, v72, 0x3b800000, v181
	v_rsq_f32_e32 v230, v72
	ds_read_b128 v[72:75], v208
	ds_read_b128 v[76:79], v208 offset:16
	ds_read_b128 v[80:83], v208 offset:32
	ds_read_b128 v[84:87], v208 offset:48
	v_pk_mul_f32 v[64:65], v[64:65], v[230:231] op_sel_hi:[1,0]
	v_pk_mul_f32 v[66:67], v[66:67], v[230:231] op_sel_hi:[1,0]
	s_waitcnt lgkmcnt(3)
	v_pk_mul_f32 v[64:65], v[72:73], v[64:65]
	v_lshlrev_b32_e32 v72, 16, v177
	v_and_b32_e32 v73, 0xffff0000, v177
	v_pk_mul_f32 v[66:67], v[74:75], v[66:67]
	v_pk_mul_f32 v[74:75], v[88:89], v[230:231] op_sel_hi:[1,0]
	v_pk_mul_f32 v[66:67], v[66:67], v[72:73]
	v_lshlrev_b32_e32 v72, 16, v178
	v_and_b32_e32 v73, 0xffff0000, v178
	s_waitcnt lgkmcnt(2)
; #define LAS __attribute__((address_space(3)))
; __device__ __forceinline__ unsigned cvt_pk_bf16(float lo, float hi) { const bf16x2_t r = __builtin_convertvector((f32x2_t){lo, hi}, bf16x2_t); return __builtin_bit_cast(unsigned, r); }
; __device__ __forceinline__ float bf_lo(unsigned w) { return __uint_as_float(w << 16); }
; __device__ __forceinline__ float bf_hi(unsigned w) { return __uint_as_float(w & 0xffff0000u); }
; __device__ __forceinline__ void gla_unit(LAS unsigned char* lds, const unsigned char* ws, const float* g_onorm, const int b, const int h, const int wv) {
;     ...
;             bf16_t* mp = mix + (t0 + t) * DM + 1024 + h * 256 + 32 * g8;
; #pragma unroll
;             for (int x = 0; x < 4; ++x) {
;                 const u32x4 og = ogr[x];
;                 const f32x4 g0 = *(const LAS f32x4*)&gon[32 * g8 + 8 * x], g1 = *(const LAS f32x4*)&gon[32 * g8 + 8 * x + 4];
;                 const float gg2[8] = {g0[0], g0[1], g0[2], g0[3], g1[0], g1[1], g1[2], g1[3]};
;                 float res[8];
; #pragma unroll
;                 for (int y = 0; y < 4; ++y) { const float a0 = bf_lo(og[y]), a1 = bf_hi(og[y]);
;                     res[2 * y] = ov[8 * x + 2 * y] * rstd * gg2[2 * y] * a0;
;                     res[2 * y + 1] = ov[8 * x + 2 * y + 1] * rstd * gg2[2 * y + 1] * a1; }
;                 u32x4 wv4; wv4[0] = cvt_pk_bf16(res[0], res[1]); wv4[1] = cvt_pk_bf16(res[2], res[3]); wv4[2] = cvt_pk_bf16(res[4], res[5]); wv4[3] = cvt_pk_bf16(res[6], res[7]);
;                 *(u32x4*)(mp + 8 * x) = wv4;
;             }
	v_pk_mul_f32 v[74:75], v[76:77], v[74:75]
	v_pk_mul_f32 v[76:77], v[90:91], v[230:231] op_sel_hi:[1,0]
	v_pk_mul_f32 v[72:73], v[74:75], v[72:73]
	v_lshlrev_b32_e32 v74, 16, v179
	v_and_b32_e32 v75, 0xffff0000, v179
	v_pk_mul_f32 v[76:77], v[78:79], v[76:77]
	v_pk_mul_f32 v[64:65], v[64:65], v[232:233]
	v_pk_mul_f32 v[74:75], v[76:77], v[74:75]
	v_add_co_u32_e32 v76, vcc, s72, v196
	v_cvt_pk_bf16_f32 v64, v64, v65
	v_cvt_pk_bf16_f32 v65, v66, v67
	v_cvt_pk_bf16_f32 v66, v72, v73
	v_cvt_pk_bf16_f32 v67, v74, v75
	v_addc_co_u32_e32 v77, vcc, 0, v197, vcc
	global_store_dwordx4 v[76:77], v[64:67], off offset:2048
	v_pk_mul_f32 v[72:73], v[94:95], v[230:231] op_sel_hi:[1,0]
	v_pk_mul_f32 v[74:75], v[192:193], v[230:231] op_sel_hi:[1,0]
	v_pk_mul_f32 v[66:67], v[92:93], v[230:231] op_sel_hi:[1,0]
	s_waitcnt vmcnt(9)
	v_lshlrev_b32_e32 v64, 16, v172
	v_and_b32_e32 v65, 0xffff0000, v172
	s_waitcnt lgkmcnt(1)
	v_pk_mul_f32 v[66:67], v[80:81], v[66:67]
	v_pk_mul_f32 v[72:73], v[82:83], v[72:73]
	v_pk_mul_f32 v[64:65], v[66:67], v[64:65]
	v_lshlrev_b32_e32 v66, 16, v173
	v_and_b32_e32 v67, 0xffff0000, v173
	v_pk_mul_f32 v[66:67], v[72:73], v[66:67]
	v_lshlrev_b32_e32 v72, 16, v174
	v_and_b32_e32 v73, 0xffff0000, v174
	s_waitcnt lgkmcnt(0)
	v_pk_mul_f32 v[74:75], v[84:85], v[74:75]
	v_pk_mul_f32 v[78:79], v[194:195], v[230:231] op_sel_hi:[1,0]
	v_pk_mul_f32 v[72:73], v[74:75], v[72:73]
	v_lshlrev_b32_e32 v74, 16, v175
	v_and_b32_e32 v75, 0xffff0000, v175
	v_pk_mul_f32 v[78:79], v[86:87], v[78:79]
	v_cvt_pk_bf16_f32 v64, v64, v65
	v_pk_mul_f32 v[74:75], v[78:79], v[74:75]
	v_cvt_pk_bf16_f32 v65, v66, v67
	v_cvt_pk_bf16_f32 v66, v72, v73
	v_cvt_pk_bf16_f32 v67, v74, v75
	global_store_dwordx4 v[76:77], v[64:67], off offset:2064
	ds_read_b128 v[64:67], v208 offset:64
	ds_read_b128 v[72:75], v208 offset:80
	v_pk_mul_f32 v[68:69], v[68:69], v[230:231] op_sel_hi:[1,0]
	v_pk_mul_f32 v[70:71], v[70:71], v[230:231] op_sel_hi:[1,0]
	v_lshlrev_b32_e32 v78, 16, v168
	s_waitcnt lgkmcnt(1)
	v_pk_mul_f32 v[64:65], v[64:65], v[68:69]
	v_lshlrev_b32_e32 v68, 16, v169
	v_and_b32_e32 v69, 0xffff0000, v169
	v_pk_mul_f32 v[66:67], v[66:67], v[70:71]
	v_pk_mul_f32 v[70:71], v[198:199], v[230:231] op_sel_hi:[1,0]
	v_pk_mul_f32 v[66:67], v[66:67], v[68:69]
	v_lshlrev_b32_e32 v68, 16, v170
	v_and_b32_e32 v69, 0xffff0000, v170
	s_waitcnt lgkmcnt(0)
	v_pk_mul_f32 v[70:71], v[72:73], v[70:71]
	v_pk_mul_f32 v[72:73], v[200:201], v[230:231] op_sel_hi:[1,0]
	v_and_b32_e32 v79, 0xffff0000, v168
	v_pk_mul_f32 v[68:69], v[70:71], v[68:69]
	v_lshlrev_b32_e32 v70, 16, v171
	v_and_b32_e32 v71, 0xffff0000, v171
	v_pk_mul_f32 v[72:73], v[74:75], v[72:73]
	v_pk_mul_f32 v[64:65], v[64:65], v[78:79]
	v_pk_mul_f32 v[70:71], v[72:73], v[70:71]
	v_cvt_pk_bf16_f32 v64, v64, v65
	v_cvt_pk_bf16_f32 v65, v66, v67
	v_cvt_pk_bf16_f32 v66, v68, v69
	v_cvt_pk_bf16_f32 v67, v70, v71
	global_store_dwordx4 v[76:77], v[64:67], off offset:2080
	ds_read_b128 v[64:67], v208 offset:96
	ds_read_b128 v[68:71], v208 offset:112
	v_pk_mul_f32 v[74:75], v[222:223], v[230:231] op_sel_hi:[1,0]
	v_lshlrev_b32_e32 v72, 16, v164
	v_and_b32_e32 v73, 0xffff0000, v164
	s_waitcnt lgkmcnt(1)
	v_pk_mul_f32 v[64:65], v[74:75], v[64:65]
	v_pk_mul_f32 v[74:75], v[224:225], v[230:231] op_sel_hi:[1,0]
	v_pk_mul_f32 v[64:65], v[64:65], v[72:73]
	v_lshlrev_b32_e32 v72, 16, v165
	v_and_b32_e32 v73, 0xffff0000, v165
	v_pk_mul_f32 v[66:67], v[74:75], v[66:67]
	v_pk_mul_f32 v[74:75], v[226:227], v[230:231] op_sel_hi:[1,0]
	v_pk_mul_f32 v[66:67], v[66:67], v[72:73]
	v_lshlrev_b32_e32 v72, 16, v166
	v_and_b32_e32 v73, 0xffff0000, v166
	s_waitcnt lgkmcnt(0)
	v_pk_mul_f32 v[68:69], v[74:75], v[68:69]
	v_pk_mul_f32 v[74:75], v[228:229], v[230:231] op_sel_hi:[1,0]
	v_pk_mul_f32 v[68:69], v[68:69], v[72:73]
	v_lshlrev_b32_e32 v72, 16, v167
	v_and_b32_e32 v73, 0xffff0000, v167
	v_pk_mul_f32 v[70:71], v[74:75], v[70:71]
	v_cvt_pk_bf16_f32 v64, v64, v65
	v_pk_mul_f32 v[70:71], v[70:71], v[72:73]
	v_cvt_pk_bf16_f32 v65, v66, v67
	v_cvt_pk_bf16_f32 v66, v68, v69
	v_cvt_pk_bf16_f32 v67, v70, v71
	global_store_dwordx4 v[76:77], v[64:67], off offset:2096
	s_cbranch_scc0 .LBB0_1712

; #define LAS __attribute__((address_space(3)))
; __device__ __forceinline__ void gla_unit(LAS unsigned char* lds, const unsigned char* ws, const float* g_onorm, const int b, const int h, const int wv) {
;     ...
;         f32x16 O[2];
; #pragma unroll
;         for (int tt = 0; tt < 2; ++tt)
; #pragma unroll
;             for (int r = 0; r < 16; ++r) O[tt][r] = 0.f;
; #pragma unroll
;         for (int et = 0; et < 4; ++et)
; #pragma unroll
;             for (int s2 = 0; s2 < 2; ++s2) {
;                 const bf16x8 sb = pack8(S[et], s2);
; #pragma unroll
;                 for (int tt = 0; tt < 2; ++tt) {
;                     const bf16x8 aq = ld2x64(qb8 + 32 * tt * QS + (32 * et + 16 * s2) * 2);
;                     O[tt] = __builtin_amdgcn_mfma_f32_32x32x16_bf16(aq, sb, O[tt], 0, 0, 0);
;                 }
;             }
;         __syncthreads();
; #pragma unroll
;         for (int pr = 0; pr < 3; ++pr) {
;             const int st = (pr == 2) ? 1 : 0, tt = (pr == 0) ? 0 : 1;
; #pragma unroll
;             for (int s2 = 0; s2 < 2; ++s2) {
;                 const bf16x8 ax = *(const LAS bf16x8*)(frb + (pr * 2 + s2) * 1024);
;                 const LAS unsigned char* vp = vP + (32 * st + 16 * s2) * VS;
;                 const bf16x8 bv = tr8(vp, vp + 8 * VS);
;                 O[tt] = __builtin_amdgcn_mfma_f32_32x32x16_bf16(ax, bv, O[tt], 0, 0, 0);
;             }
;         }
;         __builtin_amdgcn_sched_barrier(0);
; #pragma unroll
;         for (int tt = 0; tt < 2; ++tt)
; #pragma unroll
;             for (int r = 0; r < 16; ++r) ob[(32 * tt + (r & 3) + 8 * (r >> 2)) * OS] = O[tt][r];
;         __builtin_amdgcn_sched_barrier(0);
; #pragma unroll
;         for (int et = 0; et < 4; ++et)
; #pragma unroll
;             for (int rg = 0; rg < 4; ++rg) { const f32x4 dl = *(const LAS f32x4*)&decb[32 * et + 8 * rg];
.LBB0_1703:
	v_add_u32_e32 v222, v203, v202
	ds_read2_b64 v[64:67], v222 offset1:2
	v_cvt_pk_bf16_f32 v68, v48, v49
	v_cvt_pk_bf16_f32 v69, v50, v51
	v_cvt_pk_bf16_f32 v70, v52, v53
	v_cvt_pk_bf16_f32 v71, v54, v55
	v_add_u32_e32 v223, 0x2000, v222
	ds_read2_b64 v[228:231], v222 offset0:4 offset1:6
	v_cvt_pk_bf16_f32 v232, v56, v57
	v_cvt_pk_bf16_f32 v233, v58, v59
	s_waitcnt lgkmcnt(1)
	v_mfma_f32_32x32x16_bf16 v[80:95], v[64:67], v[68:71], 0
	ds_read2_b64 v[64:67], v223 offset0:64 offset1:66
	v_cvt_pk_bf16_f32 v234, v60, v61
	v_cvt_pk_bf16_f32 v235, v62, v63
	s_waitcnt lgkmcnt(1)
	s_nop 0
	v_mfma_f32_32x32x16_bf16 v[80:95], v[228:231], v[232:235], v[80:95]
	ds_read2_b64 v[228:231], v223 offset0:68 offset1:70
	s_waitcnt lgkmcnt(1)
	v_mfma_f32_32x32x16_bf16 v[64:79], v[64:67], v[68:71], 0
	s_waitcnt lgkmcnt(0)
	v_mfma_f32_32x32x16_bf16 v[64:79], v[228:231], v[232:235], v[64:79]
	ds_read2_b64 v[228:231], v222 offset0:8 offset1:10
	ds_read2_b64 v[236:239], v223 offset0:72 offset1:74
	ds_read2_b64 v[240:243], v222 offset0:12 offset1:14
	v_cvt_pk_bf16_f32 v232, v16, v17
	v_cvt_pk_bf16_f32 v233, v18, v19
	v_cvt_pk_bf16_f32 v234, v20, v21
	v_cvt_pk_bf16_f32 v235, v22, v23
	s_waitcnt lgkmcnt(2)
	s_nop 0
	v_mfma_f32_32x32x16_bf16 v[80:95], v[228:231], v[232:235], v[80:95]
	ds_read2_b64 v[248:251], v223 offset0:76 offset1:78
	s_waitcnt lgkmcnt(2)
	v_mfma_f32_32x32x16_bf16 v[64:79], v[236:239], v[232:235], v[64:79]
	ds_read2_b64 v[228:231], v222 offset0:16 offset1:18
	v_cvt_pk_bf16_f32 v232, v24, v25
	v_cvt_pk_bf16_f32 v233, v26, v27
	v_cvt_pk_bf16_f32 v234, v28, v29
	v_cvt_pk_bf16_f32 v235, v30, v31
	s_waitcnt lgkmcnt(2)
	s_nop 0
	v_mfma_f32_32x32x16_bf16 v[80:95], v[240:243], v[232:235], v[80:95]
	ds_read2_b64 v[236:239], v223 offset0:80 offset1:82
	s_waitcnt lgkmcnt(2)
	v_mfma_f32_32x32x16_bf16 v[64:79], v[248:251], v[232:235], v[64:79]
	ds_read2_b64 v[240:243], v222 offset0:20 offset1:22
	v_cvt_pk_bf16_f32 v232, v32, v33
	v_cvt_pk_bf16_f32 v233, v34, v35
	v_cvt_pk_bf16_f32 v234, v36, v37
	v_cvt_pk_bf16_f32 v235, v38, v39
	s_waitcnt lgkmcnt(2)
	s_nop 0
	v_mfma_f32_32x32x16_bf16 v[80:95], v[228:231], v[232:235], v[80:95]
	ds_read2_b64 v[248:251], v223 offset0:84 offset1:86
	s_waitcnt lgkmcnt(2)
	v_mfma_f32_32x32x16_bf16 v[64:79], v[236:239], v[232:235], v[64:79]
	ds_read2_b64 v[228:231], v222 offset0:24 offset1:26
	v_cvt_pk_bf16_f32 v232, v40, v41
	v_cvt_pk_bf16_f32 v233, v42, v43
	v_cvt_pk_bf16_f32 v234, v44, v45
	v_cvt_pk_bf16_f32 v235, v46, v47
	s_waitcnt lgkmcnt(2)
	s_nop 0
	v_mfma_f32_32x32x16_bf16 v[80:95], v[240:243], v[232:235], v[80:95]
	ds_read2_b64 v[236:239], v223 offset0:88 offset1:90
	s_waitcnt lgkmcnt(2)
	v_mfma_f32_32x32x16_bf16 v[64:79], v[248:251], v[232:235], v[64:79]
	ds_read2_b64 v[240:243], v222 offset0:28 offset1:30
	v_cvt_pk_bf16_f32 v232, v0, v1
	v_cvt_pk_bf16_f32 v233, v2, v3
	v_cvt_pk_bf16_f32 v234, v4, v5
	v_cvt_pk_bf16_f32 v235, v6, v7
	s_waitcnt lgkmcnt(2)
	s_nop 0
	v_mfma_f32_32x32x16_bf16 v[80:95], v[228:231], v[232:235], v[80:95]
	ds_read2_b64 v[248:251], v223 offset0:92 offset1:94
	s_waitcnt lgkmcnt(2)
	v_mfma_f32_32x32x16_bf16 v[64:79], v[236:239], v[232:235], v[64:79]
	v_cvt_pk_bf16_f32 v232, v8, v9
	v_cvt_pk_bf16_f32 v233, v10, v11
	v_cvt_pk_bf16_f32 v234, v12, v13
	v_cvt_pk_bf16_f32 v235, v14, v15
	s_waitcnt lgkmcnt(1)
	s_nop 0
	v_mfma_f32_32x32x16_bf16 v[80:95], v[240:243], v[232:235], v[80:95]
	s_waitcnt lgkmcnt(0)
	s_barrier
	v_mfma_f32_32x32x16_bf16 v[64:79], v[248:251], v[232:235], v[64:79]
	ds_read_b128 v[228:231], v206
	ds_read_b64_tr_b16 v[232:233], v218
	ds_read_b64_tr_b16 v[234:235], v218 offset:4608
	ds_read_b128 v[236:239], v206 offset:1024
	ds_read_b64_tr_b16 v[240:241], v218 offset:9216
	ds_read_b64_tr_b16 v[242:243], v218 offset:13824
	s_waitcnt lgkmcnt(3)
	v_mfma_f32_32x32x16_bf16 v[80:95], v[228:231], v[232:235], v[80:95]
	s_waitcnt lgkmcnt(0)
	v_mfma_f32_32x32x16_bf16 v[80:95], v[236:239], v[240:243], v[80:95]
	ds_read_b128 v[228:231], v206 offset:2048
	ds_read_b128 v[236:239], v206 offset:3072
	s_waitcnt lgkmcnt(1)
	v_mfma_f32_32x32x16_bf16 v[64:79], v[228:231], v[232:235], v[64:79]
	s_waitcnt lgkmcnt(0)
	v_mfma_f32_32x32x16_bf16 v[64:79], v[236:239], v[240:243], v[64:79]
	ds_read_b128 v[228:231], v206 offset:4096
	ds_read_b64_tr_b16 v[232:233], v218 offset:18432
	ds_read_b64_tr_b16 v[234:235], v218 offset:23040
	ds_read_b128 v[236:239], v206 offset:5120
	ds_read_b64_tr_b16 v[240:241], v218 offset:27648
	ds_read_b64_tr_b16 v[242:243], v218 offset:32256
	s_waitcnt lgkmcnt(3)
	v_mfma_f32_32x32x16_bf16 v[64:79], v[228:231], v[232:235], v[64:79]
	s_waitcnt lgkmcnt(0)
	v_mfma_f32_32x32x16_bf16 v[64:79], v[236:239], v[240:243], v[64:79]
	ds_write_b32 v207, v80
	ds_write_b32 v207, v81 offset:1040
	ds_write_b32 v207, v82 offset:2080
	ds_write_b32 v207, v83 offset:3120
	ds_write_b32 v207, v84 offset:8320
	ds_write_b32 v207, v85 offset:9360
	ds_write_b32 v207, v86 offset:10400
	ds_write_b32 v207, v87 offset:11440
	ds_write_b32 v207, v88 offset:16640
	ds_write_b32 v207, v89 offset:17680
	ds_write_b32 v207, v90 offset:18720
	ds_write_b32 v207, v91 offset:19760
	ds_write_b32 v207, v92 offset:24960
	ds_write_b32 v207, v93 offset:26000
	ds_write_b32 v207, v94 offset:27040
	ds_write_b32 v207, v95 offset:28080
	ds_write_b32 v207, v64 offset:33280
	ds_write_b32 v207, v65 offset:34320
	ds_write_b32 v207, v66 offset:35360
	ds_write_b32 v207, v67 offset:36400
	ds_write_b32 v207, v68 offset:41600
	ds_write_b32 v207, v69 offset:42640
	ds_write_b32 v207, v70 offset:43680
	ds_write_b32 v207, v71 offset:44720
	ds_write_b32 v207, v72 offset:49920
	ds_write_b32 v207, v73 offset:50960
	ds_write_b32 v207, v74 offset:52000
	ds_write_b32 v207, v75 offset:53040
	ds_write_b32 v207, v76 offset:58240
	ds_write_b32 v207, v77 offset:59280
	ds_write_b32 v207, v78 offset:60320
	ds_write_b32 v207, v79 offset:61360
	ds_read_b128 v[64:67], v205 offset:96
	ds_read_b128 v[68:71], v205 offset:64
	ds_read_b128 v[72:75], v205 offset:32
	ds_read_b128 v[76:79], v205
	s_waitcnt vmcnt(11)
; #define LAS __attribute__((address_space(3)))
; __device__ __forceinline__ void gla_unit(LAS unsigned char* lds, const unsigned char* ws, const float* g_onorm, const int b, const int h, const int wv) {
;     ...
; #pragma unroll
;         for (int et = 0; et < 4; ++et)
; #pragma unroll
;             for (int rg = 0; rg < 4; ++rg) { const f32x4 dl = *(const LAS f32x4*)&decb[32 * et + 8 * rg];
; #pragma unroll
;                 for (int x = 0; x < 4; ++x) S[et][4 * rg + x] *= dl[x]; }
; #pragma unroll
;         for (int ks = 0; ks < 4; ++ks) {
;             const LAS unsigned char* vp = vN + 16 * ks * VS;
;             const bf16x8 bv = tr8(vp, vp + 4 * VS);
; #pragma unroll
;             for (int et = 0; et < 4; ++et) {
;                 const LAS unsigned char* kp = keN + 32 * et * 2 + 16 * ks * ES;
;                 const bf16x8 ak = tr8(kp, kp + 4 * ES);
;                 S[et] = __builtin_amdgcn_mfma_f32_32x32x16_bf16(ak, bv, S[et], 0, 0, 0);
;             }
;         }
	v_lshlrev_b32_e32 v246, 16, v176
	s_waitcnt lgkmcnt(3)
	v_mul_f32_e32 v62, v62, v66
	v_mul_f32_e32 v63, v63, v67
	s_waitcnt lgkmcnt(2)
	v_mul_f32_e32 v58, v58, v70
	v_mul_f32_e32 v59, v59, v71
	v_mul_f32_e32 v60, v60, v64
	v_mul_f32_e32 v61, v61, v65
	s_waitcnt lgkmcnt(0)
	v_mul_f32_e32 v50, v50, v78
	v_mul_f32_e32 v51, v51, v79
	v_mul_f32_e32 v56, v56, v68
	v_mul_f32_e32 v57, v57, v69
	ds_read_b128 v[64:67], v205 offset:192
	ds_read_b128 v[68:71], v205 offset:224
	ds_read_b128 v[78:81], v205 offset:128
	ds_read_b128 v[82:85], v205 offset:160
	v_mul_f32_e32 v54, v54, v74
	v_mul_f32_e32 v55, v55, v75
	v_mul_f32_e32 v52, v52, v72
	v_mul_f32_e32 v53, v53, v73
	v_mul_f32_e32 v48, v48, v76
	v_mul_f32_e32 v49, v49, v77
	s_waitcnt lgkmcnt(2)
	v_mul_f32_e32 v30, v30, v70
	v_mul_f32_e32 v31, v31, v71
	v_mul_f32_e32 v26, v26, v66
	v_mul_f32_e32 v27, v27, v67
	s_waitcnt lgkmcnt(0)
	v_mul_f32_e32 v22, v22, v84
	v_mul_f32_e32 v23, v23, v85
	v_mul_f32_e32 v18, v18, v80
	v_mul_f32_e32 v19, v19, v81
	v_mul_f32_e32 v28, v28, v68
	v_mul_f32_e32 v29, v29, v69
	v_mul_f32_e32 v24, v24, v64
	v_mul_f32_e32 v25, v25, v65
	v_mul_f32_e32 v20, v20, v82
	v_mul_f32_e32 v21, v21, v83
	ds_read_b128 v[64:67], v205 offset:256
	ds_read_b128 v[68:71], v205 offset:288
	ds_read_b128 v[72:75], v205 offset:320
	ds_read_b128 v[80:83], v205 offset:352
	ds_read_b64_tr_b16 v[84:85], v219
	ds_read_b64_tr_b16 v[86:87], v219 offset:2304
	ds_read_b64_tr_b16 v[90:91], v220 offset:1280
	ds_read_b64_tr_b16 v[88:89], v220
	ds_read_b64_tr_b16 v[92:93], v220 offset:64
	ds_read_b64_tr_b16 v[228:229], v220 offset:128
	ds_read_b64_tr_b16 v[232:233], v220 offset:192
	ds_read_b64_tr_b16 v[94:95], v220 offset:1344
	ds_read_b64_tr_b16 v[230:231], v220 offset:1408
	ds_read_b64_tr_b16 v[234:235], v220 offset:1472
	ds_read_b64_tr_b16 v[236:237], v219 offset:9216
	ds_read_b64_tr_b16 v[238:239], v219 offset:11520
	s_waitcnt lgkmcnt(8)
	v_mfma_f32_32x32x16_bf16 v[48:63], v[88:91], v[84:87], v[48:63]
	v_mul_f32_e64 v16, v16, v78
	v_mul_f32_e64 v17, v17, v79
	v_mul_f32_e64 v42, v42, v74
	v_mul_f32_e64 v43, v43, v75
	v_mul_f32_e64 v38, v38, v70
	v_mul_f32_e64 v39, v39, v71
	v_mul_f32_e32 v34, v34, v66
	v_mul_f32_e32 v35, v35, v67
	v_mul_f32_e32 v44, v44, v80
	v_mul_f32_e32 v45, v45, v81
	v_mul_f32_e32 v40, v40, v72
	v_mul_f32_e32 v41, v41, v73
	ds_read_b128 v[70:73], v205 offset:448
	ds_read_b128 v[74:77], v205 offset:480
	v_mul_f32_e32 v36, v36, v68
	v_mul_f32_e32 v37, v37, v69
	ds_read_b128 v[66:69], v205 offset:384
	ds_read_b128 v[78:81], v205 offset:416
	v_mul_f32_e32 v46, v46, v82
	v_mul_f32_e32 v47, v47, v83
	v_mul_f32_e32 v32, v32, v64
	v_mul_f32_e32 v33, v33, v65
	s_waitcnt lgkmcnt(2)
	v_mul_f32_e32 v14, v14, v76
	v_mul_f32_e32 v15, v15, v77
	v_mul_f32_e32 v10, v10, v72
	v_mul_f32_e32 v11, v11, v73
	s_waitcnt lgkmcnt(0)
	v_mul_f32_e32 v6, v6, v80
	v_mul_f32_e32 v7, v7, v81
	v_mul_f32_e32 v2, v2, v68
	v_mul_f32_e32 v3, v3, v69
	v_mul_f32_e32 v12, v12, v74
	v_mul_f32_e32 v13, v13, v75
	v_mul_f32_e32 v8, v8, v70
	v_mul_f32_e32 v9, v9, v71
	v_mul_f32_e32 v4, v4, v78
	v_mul_f32_e32 v5, v5, v79
	v_mul_f32_e32 v0, v0, v66
	v_mul_f32_e32 v1, v1, v67
	v_mfma_f32_32x32x16_bf16 v[16:31], v[92:95], v[84:87], v[16:31]
	ds_read_b64_tr_b16 v[66:67], v220 offset:6400
	ds_read_b64_tr_b16 v[64:65], v220 offset:5120
	ds_read_b64_tr_b16 v[68:69], v220 offset:5184
	ds_read_b64_tr_b16 v[72:73], v220 offset:5248
	ds_read_b64_tr_b16 v[76:77], v220 offset:5312
	ds_read_b64_tr_b16 v[70:71], v220 offset:6464
	ds_read_b64_tr_b16 v[74:75], v220 offset:6528
	ds_read_b64_tr_b16 v[78:79], v220 offset:6592
	v_and_b32_e32 v247, 0xffff0000, v176
	v_mfma_f32_32x32x16_bf16 v[32:47], v[228:231], v[84:87], v[32:47]
	v_mfma_f32_32x32x16_bf16 v[0:15], v[232:235], v[84:87], v[0:15]
	s_waitcnt lgkmcnt(6)
	v_mfma_f32_32x32x16_bf16 v[48:63], v[64:67], v[236:239], v[48:63]
	s_waitcnt lgkmcnt(2)
	v_mfma_f32_32x32x16_bf16 v[16:31], v[68:71], v[236:239], v[16:31]
	s_waitcnt lgkmcnt(1)
	v_mfma_f32_32x32x16_bf16 v[32:47], v[72:75], v[236:239], v[32:47]
	s_waitcnt lgkmcnt(0)
	v_mfma_f32_32x32x16_bf16 v[0:15], v[76:79], v[236:239], v[0:15]
	ds_read_b64_tr_b16 v[64:65], v219 offset:18432
	ds_read_b64_tr_b16 v[66:67], v219 offset:20736
	ds_read_b64_tr_b16 v[70:71], v220 offset:11520
	ds_read_b64_tr_b16 v[68:69], v220 offset:10240
	ds_read_b64_tr_b16 v[72:73], v220 offset:10304
	ds_read_b64_tr_b16 v[76:77], v220 offset:10368
	ds_read_b64_tr_b16 v[80:81], v220 offset:10432
	ds_read_b64_tr_b16 v[74:75], v220 offset:11584
	ds_read_b64_tr_b16 v[78:79], v220 offset:11648
	ds_read_b64_tr_b16 v[82:83], v220 offset:11712
	ds_read_b64_tr_b16 v[84:85], v219 offset:27648
	ds_read_b64_tr_b16 v[86:87], v219 offset:29952
	s_waitcnt lgkmcnt(8)
	v_mfma_f32_32x32x16_bf16 v[48:63], v[68:71], v[64:67], v[48:63]
	ds_read_b64_tr_b16 v[68:69], v220 offset:16640
	s_waitcnt lgkmcnt(5)
	v_mfma_f32_32x32x16_bf16 v[16:31], v[72:75], v[64:67], v[16:31]
	s_waitcnt lgkmcnt(4)
	v_mfma_f32_32x32x16_bf16 v[32:47], v[76:79], v[64:67], v[32:47]
	s_waitcnt lgkmcnt(3)
	v_mfma_f32_32x32x16_bf16 v[0:15], v[80:83], v[64:67], v[0:15]
	ds_read_b64_tr_b16 v[66:67], v220 offset:15360
	ds_read_b64_tr_b16 v[70:71], v220 offset:15424
	ds_read_b64_tr_b16 v[74:75], v220 offset:15488
	ds_read_b64_tr_b16 v[78:79], v220 offset:15552
	ds_read_b64_tr_b16 v[72:73], v220 offset:16704
	ds_read_b64_tr_b16 v[76:77], v220 offset:16768
	ds_read_b64_tr_b16 v[80:81], v220 offset:16832
	s_waitcnt lgkmcnt(0)
	s_barrier
; #define LAS __attribute__((address_space(3)))
; __device__ __forceinline__ unsigned cvt_pk_bf16(float lo, float hi) { const bf16x2_t r = __builtin_convertvector((f32x2_t){lo, hi}, bf16x2_t); return __builtin_bit_cast(unsigned, r); }
; __device__ __forceinline__ float bf_lo(unsigned w) { return __uint_as_float(w << 16); }
; __device__ __forceinline__ float bf_hi(unsigned w) { return __uint_as_float(w & 0xffff0000u); }
; __device__ __forceinline__ void gla_unit(LAS unsigned char* lds, const unsigned char* ws, const float* g_onorm, const int b, const int h, const int wv) {
;     ...
;         {
;             const int t = tid >> 3, g8 = tid & 7;
;             float ov[32]; float ss = 0.f;
; #pragma unroll
;             for (int x = 0; x < 8; ++x) { const f32x4 v = *(const LAS f32x4*)&obuf[t * OS + 32 * g8 + 4 * x]; ov[4 * x] = v[0]; ov[4 * x + 1] = v[1]; ov[4 * x + 2] = v[2]; ov[4 * x + 3] = v[3];
;                 ss += v[0] * v[0] + v[1] * v[1] + v[2] * v[2] + v[3] * v[3]; }
;             ss += __builtin_bit_cast(float, __builtin_amdgcn_ds_swizzle(__builtin_bit_cast(int, ss), (1 << 10) | 0x1F)); ss += __builtin_bit_cast(float, __builtin_amdgcn_ds_swizzle(__builtin_bit_cast(int, ss), (2 << 10) | 0x1F));
;             ss += __builtin_bit_cast(float, __builtin_amdgcn_ds_swizzle(__builtin_bit_cast(int, ss), (4 << 10) | 0x1F));
;             const float rstd = __builtin_amdgcn_rsqf(ss * (1.0f / 256.0f) + EPSV);
;             bf16_t* mp = mix + (t0 + t) * DM + 1024 + h * 256 + 32 * g8;
; #pragma unroll
;             for (int x = 0; x < 4; ++x) {
;                 const u32x4 og = ogr[x];
;                 const f32x4 g0 = *(const LAS f32x4*)&gon[32 * g8 + 8 * x], g1 = *(const LAS f32x4*)&gon[32 * g8 + 8 * x + 4];
;                 const float gg2[8] = {g0[0], g0[1], g0[2], g0[3], g1[0], g1[1], g1[2], g1[3]};
;                 float res[8];
; #pragma unroll
;                 for (int y = 0; y < 4; ++y) { const float a0 = bf_lo(og[y]), a1 = bf_hi(og[y]);
;                     res[2 * y] = ov[8 * x + 2 * y] * rstd * gg2[2 * y] * a0;
;                     res[2 * y + 1] = ov[8 * x + 2 * y + 1] * rstd * gg2[2 * y + 1] * a1; }
;                 u32x4 wv4; wv4[0] = cvt_pk_bf16(res[0], res[1]); wv4[1] = cvt_pk_bf16(res[2], res[3]); wv4[2] = cvt_pk_bf16(res[4], res[5]); wv4[3] = cvt_pk_bf16(res[6], res[7]);
;                 *(u32x4*)(mp + 8 * x) = wv4;
	v_mfma_f32_32x32x16_bf16 v[48:63], v[66:69], v[84:87], v[48:63]
	ds_read_b128 v[64:67], v221
	ds_read_b128 v[88:91], v221 offset:16
	ds_read_b128 v[92:95], v221 offset:32
	ds_read_b128 v[228:231], v221 offset:48
	s_waitcnt lgkmcnt(3)
	v_mul_f32_e32 v68, v65, v65
	s_waitcnt lgkmcnt(2)
	v_mul_f32_e32 v69, v89, v89
	v_fmac_f32_e32 v68, v64, v64
	v_fmac_f32_e32 v69, v88, v88
	v_fmac_f32_e32 v68, v66, v66
	v_fmac_f32_e32 v69, v90, v90
	v_mfma_f32_32x32x16_bf16 v[16:31], v[70:73], v[84:87], v[16:31]
	v_fmac_f32_e32 v68, v67, v67
	v_fmac_f32_e32 v69, v91, v91
	s_waitcnt lgkmcnt(1)
	v_mov_b32_e32 v70, v93
	s_waitcnt lgkmcnt(0)
	v_mov_b32_e32 v71, v229
	v_add_f32_e32 v196, v68, v69
	v_mov_b32_e32 v68, v92
	v_mov_b32_e32 v69, v228
	v_pk_mul_f32 v[70:71], v[70:71], v[70:71]
	v_mov_b32_e32 v82, v95
	v_pk_fma_f32 v[68:69], v[68:69], v[68:69], v[70:71]
	v_mov_b32_e32 v70, v94
	v_mov_b32_e32 v71, v230
	v_pk_fma_f32 v[72:73], v[70:71], v[70:71], v[68:69]
	ds_read_b128 v[68:71], v221 offset:64
	ds_read_b128 v[232:235], v221 offset:80
	v_mov_b32_e32 v83, v231
	v_pk_fma_f32 v[72:73], v[82:83], v[82:83], v[72:73]
	ds_read_b128 v[236:239], v221 offset:96
	ds_read_b128 v[240:243], v221 offset:112
	v_add_f32_e32 v72, v196, v72
	s_waitcnt lgkmcnt(3)
	v_mov_b32_e32 v82, v69
	s_waitcnt lgkmcnt(2)
	v_mov_b32_e32 v83, v233
	v_add_f32_e32 v196, v72, v73
	v_mov_b32_e32 v72, v68
	v_mov_b32_e32 v73, v232
	v_pk_mul_f32 v[82:83], v[82:83], v[82:83]
	v_mfma_f32_32x32x16_bf16 v[32:47], v[74:77], v[84:87], v[32:47]
	v_fma_f32 v72, v72, v72, v82
	v_fma_f32 v73, v73, v73, v83
	v_mov_b32_e32 v82, v70
	v_mov_b32_e32 v83, v234
	v_fma_f32 v72, v82, v82, v72
	v_fma_f32 v73, v83, v83, v73
	v_mov_b32_e32 v82, v71
	v_mov_b32_e32 v83, v235
	v_pk_fma_f32 v[72:73], v[82:83], v[82:83], v[72:73]
	s_waitcnt lgkmcnt(1)
	v_mov_b32_e32 v82, v237
	v_add_f32_e32 v72, v196, v72
	s_waitcnt lgkmcnt(0)
	v_mov_b32_e32 v83, v241
	v_add_f32_e32 v196, v72, v73
	v_mov_b32_e32 v72, v236
	v_mov_b32_e32 v73, v240
	v_pk_mul_f32 v[82:83], v[82:83], v[82:83]
	v_mfma_f32_32x32x16_bf16 v[0:15], v[78:81], v[84:87], v[0:15]
	v_fma_f32 v72, v72, v72, v82
	v_fma_f32 v73, v73, v73, v83
	v_mov_b32_e32 v82, v238
	v_mov_b32_e32 v83, v242
	v_fma_f32 v72, v82, v82, v72
	v_fma_f32 v73, v83, v83, v73
	v_mov_b32_e32 v82, v239
	v_mov_b32_e32 v83, v243
	v_pk_fma_f32 v[72:73], v[82:83], v[82:83], v[72:73]
	s_nop 0
	v_add_f32_e32 v72, v196, v72
	v_add_f32_e32 v72, v72, v73
	ds_swizzle_b32 v73, v72 offset:swizzle(SWAP,1)
	v_lshl_add_u64 v[196:197], s[76:77], 0, v[188:189]
	s_waitcnt lgkmcnt(0)
	v_add_f32_e32 v72, v72, v73
	ds_swizzle_b32 v73, v72 offset:swizzle(SWAP,2)
	s_waitcnt lgkmcnt(0)
	v_add_f32_e32 v72, v72, v73
	ds_swizzle_b32 v73, v72 offset:swizzle(SWAP,4)
	s_waitcnt lgkmcnt(0)
	v_add_f32_e32 v72, v72, v73
	v_fmamk_f32 v72, v72, 0x3b800000, v181
	v_rsq_f32_e32 v244, v72
	ds_read_b128 v[72:75], v208
	ds_read_b128 v[76:79], v208 offset:16
	ds_read_b128 v[80:83], v208 offset:32
	ds_read_b128 v[84:87], v208 offset:48
	v_pk_mul_f32 v[64:65], v[64:65], v[244:245] op_sel_hi:[1,0]
	v_pk_mul_f32 v[66:67], v[66:67], v[244:245] op_sel_hi:[1,0]
	s_waitcnt lgkmcnt(3)
	v_pk_mul_f32 v[64:65], v[72:73], v[64:65]
	v_lshlrev_b32_e32 v72, 16, v177
	v_and_b32_e32 v73, 0xffff0000, v177
	v_pk_mul_f32 v[66:67], v[74:75], v[66:67]
	v_pk_mul_f32 v[74:75], v[88:89], v[244:245] op_sel_hi:[1,0]
	v_pk_mul_f32 v[66:67], v[66:67], v[72:73]
	v_lshlrev_b32_e32 v72, 16, v178
	v_and_b32_e32 v73, 0xffff0000, v178
	s_waitcnt lgkmcnt(2)
	v_pk_mul_f32 v[74:75], v[76:77], v[74:75]
	v_pk_mul_f32 v[76:77], v[90:91], v[244:245] op_sel_hi:[1,0]
	v_pk_mul_f32 v[72:73], v[74:75], v[72:73]
	v_lshlrev_b32_e32 v74, 16, v179
	v_and_b32_e32 v75, 0xffff0000, v179
	v_pk_mul_f32 v[76:77], v[78:79], v[76:77]
	v_pk_mul_f32 v[64:65], v[64:65], v[246:247]
	v_pk_mul_f32 v[74:75], v[76:77], v[74:75]
	v_add_co_u32_e32 v76, vcc, s33, v196
	v_cvt_pk_bf16_f32 v64, v64, v65
	v_cvt_pk_bf16_f32 v65, v66, v67
	v_cvt_pk_bf16_f32 v66, v72, v73
	v_cvt_pk_bf16_f32 v67, v74, v75
	v_addc_co_u32_e32 v77, vcc, 0, v197, vcc
	global_store_dwordx4 v[76:77], v[64:67], off offset:2048
	v_pk_mul_f32 v[72:73], v[94:95], v[244:245] op_sel_hi:[1,0]
	v_pk_mul_f32 v[74:75], v[228:229], v[244:245] op_sel_hi:[1,0]
	v_pk_mul_f32 v[66:67], v[92:93], v[244:245] op_sel_hi:[1,0]
	s_waitcnt vmcnt(9)
; #define LAS __attribute__((address_space(3)))
; __device__ __forceinline__ unsigned cvt_pk_bf16(float lo, float hi) { const bf16x2_t r = __builtin_convertvector((f32x2_t){lo, hi}, bf16x2_t); return __builtin_bit_cast(unsigned, r); }
; __device__ __forceinline__ float bf_lo(unsigned w) { return __uint_as_float(w << 16); }
; __device__ __forceinline__ float bf_hi(unsigned w) { return __uint_as_float(w & 0xffff0000u); }
; __device__ __forceinline__ void gla_unit(LAS unsigned char* lds, const unsigned char* ws, const float* g_onorm, const int b, const int h, const int wv) {
;     ...
;         __syncthreads();
; #pragma unroll
;         for (int i = 0; i < 2; ++i) { const int c = tid + 512 * i, row = c >> 4, cc = (c & 15) * 16;
;             *(LAS u32x4*)(lds + L_Q + row * QS + cc) = qr[par][i]; *(LAS u32x4*)(lds + L_K + row * QS + cc) = kr[par][i]; }
; #pragma unroll
;         for (int i = 0; i < 4; ++i) { const int c = tid + 512 * i; *(LAS u32x4*)(lds + L_V + (c >> 5) * VS + (c & 31) * 16) = vr[par][i]; }
;         if (tid < 32) {
;             const float L2E_ = 1.4426950408889634f;
;             *(LAS f32x4*)&dec[tid * 4] = (f32x4){__builtin_amdgcn_exp2f(dr[0] * L2E_), __builtin_amdgcn_exp2f(dr[1] * L2E_), __builtin_amdgcn_exp2f(dr[2] * L2E_), __builtin_amdgcn_exp2f(dr[3] * L2E_)};
;         }
;     ...
;             for (int x = 0; x < 4; ++x) {
;                 const u32x4 og = ogr[x];
;                 const f32x4 g0 = *(const LAS f32x4*)&gon[32 * g8 + 8 * x], g1 = *(const LAS f32x4*)&gon[32 * g8 + 8 * x + 4];
;                 const float gg2[8] = {g0[0], g0[1], g0[2], g0[3], g1[0], g1[1], g1[2], g1[3]};
;                 float res[8];
; #pragma unroll
;                 for (int y = 0; y < 4; ++y) { const float a0 = bf_lo(og[y]), a1 = bf_hi(og[y]);
;                     res[2 * y] = ov[8 * x + 2 * y] * rstd * gg2[2 * y] * a0;
;                     res[2 * y + 1] = ov[8 * x + 2 * y + 1] * rstd * gg2[2 * y + 1] * a1; }
;                 u32x4 wv4; wv4[0] = cvt_pk_bf16(res[0], res[1]); wv4[1] = cvt_pk_bf16(res[2], res[3]); wv4[2] = cvt_pk_bf16(res[4], res[5]); wv4[3] = cvt_pk_bf16(res[6], res[7]);
;                 *(u32x4*)(mp + 8 * x) = wv4;
	v_lshlrev_b32_e32 v64, 16, v172
	v_and_b32_e32 v65, 0xffff0000, v172
	s_waitcnt lgkmcnt(1)
	v_pk_mul_f32 v[66:67], v[80:81], v[66:67]
	v_pk_mul_f32 v[72:73], v[82:83], v[72:73]
	v_pk_mul_f32 v[64:65], v[66:67], v[64:65]
	v_lshlrev_b32_e32 v66, 16, v173
	v_and_b32_e32 v67, 0xffff0000, v173
	v_pk_mul_f32 v[66:67], v[72:73], v[66:67]
	v_lshlrev_b32_e32 v72, 16, v174
	v_and_b32_e32 v73, 0xffff0000, v174
	s_waitcnt lgkmcnt(0)
	v_pk_mul_f32 v[74:75], v[84:85], v[74:75]
	v_pk_mul_f32 v[78:79], v[230:231], v[244:245] op_sel_hi:[1,0]
	v_pk_mul_f32 v[72:73], v[74:75], v[72:73]
	v_lshlrev_b32_e32 v74, 16, v175
	v_and_b32_e32 v75, 0xffff0000, v175
	v_pk_mul_f32 v[78:79], v[86:87], v[78:79]
	v_cvt_pk_bf16_f32 v64, v64, v65
	v_pk_mul_f32 v[74:75], v[78:79], v[74:75]
	v_cvt_pk_bf16_f32 v65, v66, v67
	v_cvt_pk_bf16_f32 v66, v72, v73
	v_cvt_pk_bf16_f32 v67, v74, v75
	global_store_dwordx4 v[76:77], v[64:67], off offset:2064
	ds_read_b128 v[64:67], v208 offset:64
	ds_read_b128 v[72:75], v208 offset:80
	v_pk_mul_f32 v[68:69], v[68:69], v[244:245] op_sel_hi:[1,0]
	v_pk_mul_f32 v[70:71], v[70:71], v[244:245] op_sel_hi:[1,0]
	v_lshlrev_b32_e32 v78, 16, v168
	s_waitcnt lgkmcnt(1)
	v_pk_mul_f32 v[64:65], v[64:65], v[68:69]
	v_lshlrev_b32_e32 v68, 16, v169
	v_and_b32_e32 v69, 0xffff0000, v169
	v_pk_mul_f32 v[66:67], v[66:67], v[70:71]
	v_pk_mul_f32 v[70:71], v[232:233], v[244:245] op_sel_hi:[1,0]
	v_pk_mul_f32 v[66:67], v[66:67], v[68:69]
	v_lshlrev_b32_e32 v68, 16, v170
	v_and_b32_e32 v69, 0xffff0000, v170
	s_waitcnt lgkmcnt(0)
	v_pk_mul_f32 v[70:71], v[72:73], v[70:71]
	v_pk_mul_f32 v[72:73], v[234:235], v[244:245] op_sel_hi:[1,0]
	v_and_b32_e32 v79, 0xffff0000, v168
	v_pk_mul_f32 v[68:69], v[70:71], v[68:69]
	v_lshlrev_b32_e32 v70, 16, v171
	v_and_b32_e32 v71, 0xffff0000, v171
	v_pk_mul_f32 v[72:73], v[74:75], v[72:73]
	v_pk_mul_f32 v[64:65], v[64:65], v[78:79]
	v_pk_mul_f32 v[70:71], v[72:73], v[70:71]
	v_cvt_pk_bf16_f32 v64, v64, v65
	v_cvt_pk_bf16_f32 v65, v66, v67
	v_cvt_pk_bf16_f32 v66, v68, v69
	v_cvt_pk_bf16_f32 v67, v70, v71
	global_store_dwordx4 v[76:77], v[64:67], off offset:2080
	ds_read_b128 v[64:67], v208 offset:96
	ds_read_b128 v[68:71], v208 offset:112
	v_pk_mul_f32 v[74:75], v[236:237], v[244:245] op_sel_hi:[1,0]
	v_lshlrev_b32_e32 v72, 16, v164
	v_and_b32_e32 v73, 0xffff0000, v164
	s_waitcnt lgkmcnt(1)
	v_pk_mul_f32 v[64:65], v[74:75], v[64:65]
	v_pk_mul_f32 v[74:75], v[238:239], v[244:245] op_sel_hi:[1,0]
	v_pk_mul_f32 v[64:65], v[64:65], v[72:73]
	v_lshlrev_b32_e32 v72, 16, v165
	v_and_b32_e32 v73, 0xffff0000, v165
	v_pk_mul_f32 v[66:67], v[74:75], v[66:67]
	v_pk_mul_f32 v[74:75], v[240:241], v[244:245] op_sel_hi:[1,0]
	v_pk_mul_f32 v[66:67], v[66:67], v[72:73]
	v_lshlrev_b32_e32 v72, 16, v166
	v_and_b32_e32 v73, 0xffff0000, v166
	s_waitcnt lgkmcnt(0)
	v_pk_mul_f32 v[68:69], v[74:75], v[68:69]
	v_pk_mul_f32 v[74:75], v[242:243], v[244:245] op_sel_hi:[1,0]
	v_pk_mul_f32 v[68:69], v[68:69], v[72:73]
	v_lshlrev_b32_e32 v72, 16, v167
	v_and_b32_e32 v73, 0xffff0000, v167
	v_pk_mul_f32 v[70:71], v[74:75], v[70:71]
	v_cvt_pk_bf16_f32 v64, v64, v65
	v_pk_mul_f32 v[70:71], v[70:71], v[72:73]
	v_cvt_pk_bf16_f32 v65, v66, v67
	v_cvt_pk_bf16_f32 v66, v68, v69
	v_cvt_pk_bf16_f32 v67, v70, v71
	global_store_dwordx4 v[76:77], v[64:67], off offset:2096
	s_barrier
	s_waitcnt vmcnt(20)
	ds_write_b128 v209, v[132:135]
	ds_write_b128 v209, v[136:139] offset:17408
	ds_write_b128 v210, v[140:143]
	ds_write_b128 v210, v[144:147] offset:17408
	ds_write_b128 v211, v[148:151]
	ds_write_b128 v212, v[152:155]
	ds_write_b128 v213, v[156:159]
	ds_write_b128 v214, v[160:163]
	s_and_saveexec_b64 s[42:43], s[0:1]
	s_cbranch_execz .LBB0_1705
	s_waitcnt vmcnt(12)
	v_mul_f32_e32 v64, 0x3fb8aa3b, v128
	v_mul_f32_e32 v65, 0x3fb8aa3b, v129
	v_mul_f32_e32 v66, 0x3fb8aa3b, v130
	v_mul_f32_e32 v67, 0x3fb8aa3b, v131
	v_exp_f32_e32 v64, v64
	v_exp_f32_e32 v65, v65
	v_exp_f32_e32 v66, v66
	v_exp_f32_e32 v67, v67
	ds_write_b128 v226, v[64:67]
